# speedup vs baseline: 1.0374x; 1.0022x over previous
.LBB3_45:
	v_add_u32_e32 v238, 0x12600, v137
	ds_read_b128 v[196:199], v238
	ds_read_b64 v[200:201], v238 offset:32
	ds_read_b128 v[202:205], v238 offset:16
	ds_read_b64 v[206:207], v238 offset:96
	ds_read_b128 v[208:211], v238 offset:80
	ds_read_b128 v[212:215], v238 offset:64
	ds_read_b64 v[216:217], v238 offset:544
	ds_read_b128 v[218:221], v238 offset:512
	ds_read_b128 v[222:225], v238 offset:528
	ds_read_b64 v[226:227], v238 offset:608
	ds_read_b128 v[228:231], v238 offset:592
	ds_read_b128 v[232:235], v238 offset:576
	v_add_u32_e32 v100, 0, v194
	s_nop 0
	ds_read_b128 v[96:99], v100
	ds_read_b128 v[100:103], v100 offset:2048
	s_waitcnt lgkmcnt(1)
	v_mfma_f32_16x16x32_f16 v[104:107], v[96:99], v[36:39], 0
	v_mfma_f32_16x16x32_f16 v[108:111], v[96:99], v[52:55], 0
	v_mfma_f32_16x16x32_f16 v[112:115], v[96:99], v[68:71], 0
	v_mfma_f32_16x16x32_f16 v[116:119], v[96:99], v[84:87], 0
	v_add_u32_e32 v96, 0, v195
	ds_read_b128 v[124:127], v96
	ds_read_b128 v[128:131], v96 offset:2048
	s_waitcnt lgkmcnt(1)
	v_mfma_f32_16x16x32_f16 v[120:123], v[124:127], v[44:47], v[104:107]
	v_mfma_f32_16x16x32_f16 v[108:111], v[124:127], v[60:63], v[108:111]
	v_mfma_f32_16x16x32_f16 v[96:99], v[124:127], v[76:79], v[112:115]
	v_mfma_f32_16x16x32_f16 v[142:145], v[124:127], v[92:95], v[116:119]
	v_mfma_f32_16x16x32_f16 v[104:107], v[100:103], v[36:39], 0
	v_mfma_f32_16x16x32_f16 v[112:115], v[100:103], v[52:55], 0
	v_mfma_f32_16x16x32_f16 v[124:127], v[100:103], v[68:71], 0
	v_mfma_f32_16x16x32_f16 v[132:135], v[100:103], v[84:87], 0
	s_waitcnt lgkmcnt(0)
	v_mfma_f32_16x16x32_f16 v[116:119], v[128:131], v[44:47], v[104:107]
	v_mfma_f32_16x16x32_f16 v[112:115], v[128:131], v[60:63], v[112:115]
	v_mfma_f32_16x16x32_f16 v[100:103], v[128:131], v[76:79], v[124:127]
	v_mfma_f32_16x16x32_f16 v[128:131], v[128:131], v[92:95], v[132:135]
	v_add_u32_e32 v140, 0, v137
	v_add_u32_e32 v104, 0x12600, v140
	s_nop 0
	v_add_u32_e32 v124, 0x12620, v140
	s_nop 0
	v_add_u32_e32 v124, 0x12610, v140
	s_nop 0
	s_waitcnt lgkmcnt(2)
	v_fma_f32 v132, v196, v120, v108
	v_fma_f32 v132, -v197, v121, v132
	v_fma_f32 v133, v196, v121, v109
	v_fmac_f32_e32 v133, v197, v120
	v_fma_f32 v134, v196, v132, v96
	v_fma_f32 v134, -v197, v133, v134
	v_fma_f32 v133, v196, v133, v97
	v_fmac_f32_e32 v133, v197, v132
	v_fma_f32 v132, v196, v134, v142
	v_fma_f32 v132, -v197, v133, v132
	v_fma_f32 v143, v196, v133, v143
	v_fmac_f32_e32 v143, v197, v134
	v_mov_b32_dpp v133, v132 row_shr:1 row_mask:0xf bank_mask:0xf bound_ctrl:1
	v_fmac_f32_e32 v132, v198, v133
	v_mov_b32_dpp v134, v143 row_shr:1 row_mask:0xf bank_mask:0xf bound_ctrl:1
	v_fma_f32 v132, -v199, v134, v132
	v_fmac_f32_e32 v143, v198, v134
	v_fmac_f32_e32 v143, v199, v133
	v_mov_b32_dpp v106, v132 row_shr:2 row_mask:0xf bank_mask:0xf bound_ctrl:1
	v_add_u32_e32 v133, 0x12660, v140
	v_mov_b32_dpp v107, v143 row_shr:2 row_mask:0xf bank_mask:0xf bound_ctrl:1
	s_nop 0
	s_waitcnt lgkmcnt(1)
	v_fmac_f32_e32 v132, v202, v106
	v_fma_f32 v132, -v203, v107, v132
	v_fmac_f32_e32 v143, v202, v107
	v_fmac_f32_e32 v143, v203, v106
	v_mov_b32_dpp v106, v132 row_shr:4 row_mask:0xf bank_mask:0xf bound_ctrl:1
	v_fmac_f32_e32 v132, v204, v106
	v_mov_b32_dpp v107, v143 row_shr:4 row_mask:0xf bank_mask:0xf bound_ctrl:1
	v_fma_f32 v124, -v205, v107, v132
	v_fmac_f32_e32 v143, v204, v107
	v_fmac_f32_e32 v143, v205, v106
	v_mov_b32_dpp v106, v124 row_shr:8 row_mask:0xf bank_mask:0xf bound_ctrl:1
	v_fmac_f32_e32 v124, v200, v106
	v_mov_b32_dpp v107, v143 row_shr:8 row_mask:0xf bank_mask:0xf bound_ctrl:1
	v_fma_f32 v142, -v201, v107, v124
	v_add_u32_e32 v124, 0x12640, v140
	v_add_u32_e32 v125, 0x12650, v140
	s_nop 0
	s_nop 0
	v_fmac_f32_e32 v143, v200, v107
	v_fmac_f32_e32 v143, v201, v106
	v_xor_b32_e32 v141, 0x80000000, v197
	v_mov_b32_dpp v142, v142 row_shr:1 row_mask:0xf bank_mask:0xf bound_ctrl:1
	s_waitcnt lgkmcnt(0)
	v_fma_f32 v106, v212, v122, v110
	v_fma_f32 v106, -v213, v123, v106
	v_fma_f32 v146, v212, v123, v111
	v_fmac_f32_e32 v146, v213, v122
	v_fma_f32 v147, v212, v106, v98
	v_fma_f32 v147, -v213, v146, v147
	v_fma_f32 v146, v212, v146, v99
	v_fmac_f32_e32 v146, v213, v106
	v_fma_f32 v106, v212, v147, v144
	v_fma_f32 v106, -v213, v146, v106
	v_fmac_f32_e32 v145, v212, v146
	v_fmac_f32_e32 v145, v213, v147
	v_mov_b32_dpp v144, v106 row_shr:1 row_mask:0xf bank_mask:0xf bound_ctrl:1
	v_fmac_f32_e32 v106, v214, v144
	v_mov_b32_dpp v146, v145 row_shr:1 row_mask:0xf bank_mask:0xf bound_ctrl:1
	v_fma_f32 v106, -v215, v146, v106
	v_fmac_f32_e32 v145, v214, v146
	v_fmac_f32_e32 v145, v215, v144
	v_mov_b32_dpp v126, v106 row_shr:2 row_mask:0xf bank_mask:0xf bound_ctrl:1
	v_fmac_f32_e32 v106, v208, v126
	v_mov_b32_dpp v127, v145 row_shr:2 row_mask:0xf bank_mask:0xf bound_ctrl:1
	v_fma_f32 v106, -v209, v127, v106
	v_fmac_f32_e32 v145, v208, v127
	v_fmac_f32_e32 v145, v209, v126
	v_mov_b32_dpp v126, v106 row_shr:4 row_mask:0xf bank_mask:0xf bound_ctrl:1
	v_fmac_f32_e32 v106, v210, v126
	v_mov_b32_dpp v127, v145 row_shr:4 row_mask:0xf bank_mask:0xf bound_ctrl:1
	v_fma_f32 v106, -v211, v127, v106
	v_fmac_f32_e32 v145, v210, v127
	v_fmac_f32_e32 v145, v211, v126
	v_mov_b32_dpp v126, v106 row_shr:8 row_mask:0xf bank_mask:0xf bound_ctrl:1
	v_fmac_f32_e32 v106, v206, v126
	v_mov_b32_dpp v127, v145 row_shr:8 row_mask:0xf bank_mask:0xf bound_ctrl:1
	v_fma_f32 v106, -v207, v127, v106
	v_fmac_f32_e32 v145, v206, v127
	v_add_u32_e32 v127, 0x12820, v140
	v_fmac_f32_e32 v145, v207, v126
	v_add_u32_e32 v126, 0x12800, v140
	s_nop 0
	s_nop 0
	v_mov_b32_dpp v150, v106 row_shr:1 row_mask:0xf bank_mask:0xf bound_ctrl:1
	v_add_u32_e32 v106, 0x12810, v140
	v_mov_b32_dpp v151, v145 row_shr:1 row_mask:0xf bank_mask:0xf bound_ctrl:1
	s_nop 0
	s_waitcnt lgkmcnt(1)
	v_fma_f32 v106, v218, v116, v112
	v_fma_f32 v106, -v219, v117, v106
	v_fma_f32 v126, v218, v117, v113
	v_fmac_f32_e32 v126, v219, v116
	v_fma_f32 v127, v218, v106, v100
	v_fma_f32 v127, -v219, v126, v127
	v_fma_f32 v126, v218, v126, v101
	v_fmac_f32_e32 v126, v219, v106
	v_fma_f32 v152, v218, v126, v129
	v_fma_f32 v106, v218, v127, v128
	v_fmac_f32_e32 v152, v219, v127
	v_fma_f32 v106, -v219, v126, v106
	v_add_u32_e32 v128, 0x12860, v140
	v_mov_b32_dpp v127, v152 row_shr:1 row_mask:0xf bank_mask:0xf bound_ctrl:1
	v_mov_b32_dpp v126, v106 row_shr:1 row_mask:0xf bank_mask:0xf bound_ctrl:1
	v_fmac_f32_e32 v152, v220, v127
	v_fmac_f32_e32 v106, v220, v126
	v_fmac_f32_e32 v152, v221, v126
	v_fma_f32 v106, -v221, v127, v106
	s_nop 0
	v_mov_b32_dpp v127, v152 row_shr:2 row_mask:0xf bank_mask:0xf bound_ctrl:1
	v_mov_b32_dpp v126, v106 row_shr:2 row_mask:0xf bank_mask:0xf bound_ctrl:1
	s_waitcnt lgkmcnt(1)
	v_fmac_f32_e32 v152, v222, v127
	v_fmac_f32_e32 v106, v222, v126
	v_fmac_f32_e32 v152, v223, v126
	v_fma_f32 v106, -v223, v127, v106
	v_add_u32_e32 v144, 0x12840, v140
	v_mov_b32_dpp v127, v152 row_shr:4 row_mask:0xf bank_mask:0xf bound_ctrl:1
	v_mov_b32_dpp v126, v106 row_shr:4 row_mask:0xf bank_mask:0xf bound_ctrl:1
	v_fmac_f32_e32 v152, v224, v127
	v_fmac_f32_e32 v106, v224, v126
	v_fmac_f32_e32 v152, v225, v126
	v_add_u32_e32 v126, 0x12850, v140
	v_fma_f32 v106, -v225, v127, v106
	s_nop 0
	s_nop 0
	v_mov_b32_dpp v154, v106 row_shr:8 row_mask:0xf bank_mask:0xf bound_ctrl:1
	v_mov_b32_dpp v155, v152 row_shr:8 row_mask:0xf bank_mask:0xf bound_ctrl:1
	v_fmac_f32_e32 v106, v216, v154
	v_fma_f32 v106, -v217, v155, v106
	v_fmac_f32_e32 v152, v216, v155
	v_fmac_f32_e32 v152, v217, v154
	v_mov_b32_dpp v148, v106 row_shr:1 row_mask:0xf bank_mask:0xf bound_ctrl:1
	s_waitcnt lgkmcnt(0)
	v_fma_f32 v106, v232, v118, v114
	v_fma_f32 v106, -v233, v119, v106
	v_fma_f32 v140, v232, v119, v115
	v_mov_b32_dpp v149, v152 row_shr:1 row_mask:0xf bank_mask:0xf bound_ctrl:1
	v_fmac_f32_e32 v140, v233, v118
	v_fma_f32 v152, v232, v106, v102
	v_fma_f32 v152, -v233, v140, v152
	v_fma_f32 v140, v232, v140, v103
	v_fmac_f32_e32 v140, v233, v106
	v_fma_f32 v106, v232, v152, v130
	v_fmac_f32_e32 v131, v232, v140
	v_fma_f32 v106, -v233, v140, v106
	v_fmac_f32_e32 v131, v233, v152
	v_mov_b32_dpp v143, v143 row_shr:1 row_mask:0xf bank_mask:0xf bound_ctrl:1
	v_mov_b32_dpp v130, v106 row_shr:1 row_mask:0xf bank_mask:0xf bound_ctrl:1
	v_mov_b32_dpp v140, v131 row_shr:1 row_mask:0xf bank_mask:0xf bound_ctrl:1
	v_fmac_f32_e32 v106, v234, v130
	v_fmac_f32_e32 v131, v234, v140
	v_fma_f32 v106, -v235, v140, v106
	v_fmac_f32_e32 v131, v235, v130
	v_xor_b32_e32 v107, 0x80000000, v213
	v_mov_b32_dpp v130, v106 row_shr:2 row_mask:0xf bank_mask:0xf bound_ctrl:1
	v_mov_b32_dpp v140, v131 row_shr:2 row_mask:0xf bank_mask:0xf bound_ctrl:1
	v_fmac_f32_e32 v106, v228, v130
	v_fmac_f32_e32 v131, v228, v140
	v_fma_f32 v106, -v229, v140, v106
	v_fmac_f32_e32 v131, v229, v130
	v_xor_b32_e32 v153, 0x80000000, v219
	v_mov_b32_dpp v126, v106 row_shr:4 row_mask:0xf bank_mask:0xf bound_ctrl:1
	v_mov_b32_dpp v127, v131 row_shr:4 row_mask:0xf bank_mask:0xf bound_ctrl:1
	v_fmac_f32_e32 v106, v230, v126
	v_fmac_f32_e32 v131, v230, v127
	v_fma_f32 v106, -v231, v127, v106
	v_fmac_f32_e32 v131, v231, v126
	v_xor_b32_e32 v155, 0x80000000, v233
	v_mov_b32_dpp v126, v106 row_shr:8 row_mask:0xf bank_mask:0xf bound_ctrl:1
	v_mov_b32_dpp v127, v131 row_shr:8 row_mask:0xf bank_mask:0xf bound_ctrl:1
	v_fmac_f32_e32 v106, v226, v126
	v_fmac_f32_e32 v131, v226, v127
	v_fma_f32 v106, -v227, v127, v106
	v_fmac_f32_e32 v131, v227, v126
	s_nop 0
	v_mov_b32_dpp v126, v106 row_shr:1 row_mask:0xf bank_mask:0xf bound_ctrl:1
	v_mov_b32_dpp v127, v131 row_shr:1 row_mask:0xf bank_mask:0xf bound_ctrl:1
	v_pk_fma_f32 v[120:121], v[196:197], v[142:143], v[120:121] op_sel_hi:[0,1,1]
	v_pk_fma_f32 v[128:129], v[218:219], v[148:149], v[116:117] op_sel_hi:[0,1,1]
	v_pk_fma_f32 v[122:123], v[212:213], v[150:151], v[122:123] op_sel_hi:[0,1,1]
	v_pk_fma_f32 v[130:131], v[232:233], v[126:127], v[118:119] op_sel_hi:[0,1,1]
	v_cvt_pk_f16_f32 v119, v126, v127
	v_add_u32_e32 v134, s0, v189
	v_pk_fma_f32 v[120:121], v[196:197], v[142:143], v[120:121] op_sel:[1,0,1] op_sel_hi:[1,1,0] neg_hi:[1,0,0]
	v_pk_fma_f32 v[128:129], v[218:219], v[148:149], v[128:129] op_sel:[1,0,1] op_sel_hi:[1,1,0] neg_hi:[1,0,0]
	v_pk_fma_f32 v[122:123], v[212:213], v[150:151], v[122:123] op_sel:[1,0,1] op_sel_hi:[1,1,0] neg_hi:[1,0,0]
	v_pk_fma_f32 v[126:127], v[232:233], v[126:127], v[130:131] op_sel:[1,0,1] op_sel_hi:[1,1,0] neg_hi:[1,0,0]
	v_mov_b32_e32 v140, v197
	v_mov_b32_e32 v152, v219
	v_mov_b32_e32 v106, v213
	v_mov_b32_e32 v154, v233
	v_cvt_pk_f16_f32 v116, v142, v143
	v_xor_b32_e32 v142, v134, v188
	v_pk_fma_f32 v[130:131], v[196:197], v[120:121], v[108:109] op_sel:[0,1,0] op_sel_hi:[0,0,1]
	v_pk_fma_f32 v[112:113], v[218:219], v[128:129], v[112:113] op_sel:[0,1,0] op_sel_hi:[0,0,1]
	v_pk_fma_f32 v[134:135], v[212:213], v[122:123], v[110:111] op_sel:[0,1,0] op_sel_hi:[0,0,1]
	v_pk_fma_f32 v[114:115], v[232:233], v[126:127], v[114:115] op_sel:[0,1,0] op_sel_hi:[0,0,1]
	v_cvt_pk_f16_f32 v111, v127, v126
	v_cvt_pk_f16_f32 v110, v129, v128
	v_lshl_add_u32 v142, v142, 4, v190
	v_pk_fma_f32 v[130:131], v[140:141], v[120:121], v[130:131] op_sel:[1,0,0] op_sel_hi:[0,1,1]
	v_pk_fma_f32 v[128:129], v[152:153], v[128:129], v[112:113] op_sel:[1,0,0] op_sel_hi:[0,1,1]
	v_pk_fma_f32 v[106:107], v[106:107], v[122:123], v[134:135] op_sel:[1,0,0] op_sel_hi:[0,1,1]
	v_pk_fma_f32 v[126:127], v[154:155], v[126:127], v[114:115] op_sel:[1,0,0] op_sel_hi:[0,1,1]
	v_cvt_pk_f16_f32 v109, v123, v122
	v_cvt_pk_f16_f32 v108, v121, v120
	ds_read_b128 v[112:115], v142 offset:32768
	ds_read_b128 v[120:123], v142 offset:36864
	v_pk_fma_f32 v[134:135], v[196:197], v[130:131], v[96:97] op_sel_hi:[0,1,1]
	v_pk_fma_f32 v[100:101], v[218:219], v[128:129], v[100:101] op_sel_hi:[0,1,1]
	v_pk_fma_f32 v[140:141], v[212:213], v[106:107], v[98:99] op_sel_hi:[0,1,1]
	v_pk_fma_f32 v[102:103], v[232:233], v[126:127], v[102:103] op_sel_hi:[0,1,1]
	v_cvt_pk_f16_f32 v97, v106, v107
	v_pk_fma_f32 v[104:105], v[196:197], v[130:131], v[134:135] op_sel:[1,0,1] op_sel_hi:[1,1,0] neg_hi:[1,0,0]
	v_pk_fma_f32 v[100:101], v[218:219], v[128:129], v[100:101] op_sel:[1,0,1] op_sel_hi:[1,1,0] neg_hi:[1,0,0]
	v_pk_fma_f32 v[106:107], v[212:213], v[106:107], v[140:141] op_sel:[1,0,1] op_sel_hi:[1,1,0] neg_hi:[1,0,0]
	v_pk_fma_f32 v[102:103], v[232:233], v[126:127], v[102:103] op_sel:[1,0,1] op_sel_hi:[1,1,0] neg_hi:[1,0,0]
	v_cvt_pk_f16_f32 v104, v104, v105
	v_cvt_pk_f16_f32 v105, v100, v101
	v_cvt_pk_f16_f32 v100, v106, v107
	v_cvt_pk_f16_f32 v103, v102, v103
	v_cvt_pk_f16_f32 v118, v148, v149
	v_cvt_pk_f16_f32 v117, v150, v151
	v_cvt_pk_f16_f32 v99, v126, v127
	v_cvt_pk_f16_f32 v98, v128, v129
	v_cvt_pk_f16_f32 v96, v130, v131
	v_alignbit_b32 v101, v100, v100, 16
	v_alignbit_b32 v100, v104, v104, 16
	v_alignbit_b32 v102, v105, v105, 16
	v_alignbit_b32 v103, v103, v103, 16
	s_waitcnt lgkmcnt(1)
	v_mfma_f32_16x16x32_f16 v[88:91], v[112:115], v[116:119], v[88:91]
	s_add_i32 s0, s0, 4
	v_add_u32_e32 v137, 0x400, v137
	v_add_u32_e32 v194, 0x1000, v194
	v_mfma_f32_16x16x32_f16 v[80:83], v[112:115], v[108:111], v[80:83]
	s_cmp_lg_u32 s0, 16
	v_add_u32_e32 v195, 0x1000, v195
	v_mfma_f32_16x16x32_f16 v[72:75], v[112:115], v[96:99], v[72:75]
	v_mfma_f32_16x16x32_f16 v[64:67], v[112:115], v[100:103], v[64:67]
	ds_read_b128 v[104:107], v142 offset:40960
	ds_read_b128 v[112:115], v142 offset:45056
	s_waitcnt lgkmcnt(2)
	v_mfma_f32_16x16x32_f16 v[56:59], v[120:123], v[116:119], v[56:59]
	v_mfma_f32_16x16x32_f16 v[48:51], v[120:123], v[108:111], v[48:51]
	v_mfma_f32_16x16x32_f16 v[40:43], v[120:123], v[96:99], v[40:43]
	v_mfma_f32_16x16x32_f16 v[32:35], v[120:123], v[100:103], v[32:35]
	s_waitcnt lgkmcnt(1)
	v_mfma_f32_16x16x32_f16 v[28:31], v[104:107], v[116:119], v[28:31]
	v_mfma_f32_16x16x32_f16 v[24:27], v[104:107], v[108:111], v[24:27]
	v_mfma_f32_16x16x32_f16 v[20:23], v[104:107], v[96:99], v[20:23]
	v_mfma_f32_16x16x32_f16 v[16:19], v[104:107], v[100:103], v[16:19]
	s_waitcnt lgkmcnt(0)
	v_mfma_f32_16x16x32_f16 v[12:15], v[112:115], v[116:119], v[12:15]
	v_mfma_f32_16x16x32_f16 v[8:11], v[112:115], v[108:111], v[8:11]
	v_mfma_f32_16x16x32_f16 v[4:7], v[112:115], v[96:99], v[4:7]
	v_mfma_f32_16x16x32_f16 v[0:3], v[112:115], v[100:103], v[0:3]
	s_cbranch_scc1 .LBB3_45
	s_mov_b32 s0, 0
.LBB3_47:
	v_add_u32_e32 v238, 0x12600, v179
	ds_read_b128 v[196:199], v238
	ds_read_b64 v[200:201], v238 offset:32
	ds_read_b128 v[202:205], v238 offset:16
	ds_read_b64 v[206:207], v238 offset:96
	ds_read_b128 v[208:211], v238 offset:80
	ds_read_b128 v[212:215], v238 offset:64
	ds_read_b64 v[216:217], v238 offset:544
	ds_read_b128 v[218:221], v238 offset:512
	ds_read_b128 v[222:225], v238 offset:528
	ds_read_b64 v[226:227], v238 offset:608
	ds_read_b128 v[228:231], v238 offset:592
	ds_read_b128 v[232:235], v238 offset:576
	v_add_u32_e32 v100, 0, v175
	ds_read_b128 v[96:99], v100
	ds_read_b128 v[100:103], v100 offset:2048
	s_waitcnt lgkmcnt(1)
	v_mfma_f32_16x16x32_f16 v[104:107], v[96:99], v[36:39], 0
	v_mfma_f32_16x16x32_f16 v[108:111], v[96:99], v[52:55], 0
	v_mfma_f32_16x16x32_f16 v[112:115], v[96:99], v[68:71], 0
	v_mfma_f32_16x16x32_f16 v[116:119], v[96:99], v[84:87], 0
	v_add_u32_e32 v96, 0, v174
	ds_read_b128 v[120:123], v96
	ds_read_b128 v[124:127], v96 offset:2048
	s_waitcnt lgkmcnt(1)
	v_mfma_f32_16x16x32_f16 v[132:135], v[120:123], v[44:47], v[104:107]
	v_mfma_f32_16x16x32_f16 v[96:99], v[120:123], v[60:63], v[108:111]
	v_mfma_f32_16x16x32_f16 v[104:107], v[120:123], v[76:79], v[112:115]
	v_mfma_f32_16x16x32_f16 v[120:123], v[120:123], v[92:95], v[116:119]
	v_mfma_f32_16x16x32_f16 v[108:111], v[100:103], v[36:39], 0
	v_mfma_f32_16x16x32_f16 v[112:115], v[100:103], v[52:55], 0
	v_mfma_f32_16x16x32_f16 v[116:119], v[100:103], v[68:71], 0
	v_mfma_f32_16x16x32_f16 v[140:143], v[100:103], v[84:87], 0
	s_waitcnt lgkmcnt(0)
	v_mfma_f32_16x16x32_f16 v[128:131], v[124:127], v[44:47], v[108:111]
	v_mfma_f32_16x16x32_f16 v[100:103], v[124:127], v[60:63], v[112:115]
	v_mfma_f32_16x16x32_f16 v[112:115], v[124:127], v[76:79], v[116:119]
	v_mfma_f32_16x16x32_f16 v[116:119], v[124:127], v[92:95], v[140:143]
	v_add_u32_e32 v137, 0, v179
	v_add_u32_e32 v108, 0x12600, v137
	s_nop 0
	v_add_u32_e32 v124, 0x12620, v137
	s_nop 0
	v_add_u32_e32 v124, 0x12610, v137
	s_nop 0
	s_waitcnt lgkmcnt(2)
	v_fma_f32 v140, v196, v120, v104
	v_fma_f32 v140, -v197, v121, v140
	v_fma_f32 v141, v196, v121, v105
	v_fmac_f32_e32 v141, v197, v120
	v_fma_f32 v142, v196, v140, v96
	v_fma_f32 v142, -v197, v141, v142
	v_fma_f32 v141, v196, v141, v97
	v_fmac_f32_e32 v141, v197, v140
	v_fma_f32 v132, v196, v142, v132
	v_fma_f32 v132, -v197, v141, v132
	v_fma_f32 v146, v196, v141, v133
	v_fmac_f32_e32 v146, v197, v142
	v_mov_b32_dpp v133, v132 row_shl:1 row_mask:0xf bank_mask:0xf bound_ctrl:1
	v_fmac_f32_e32 v132, v198, v133
	v_mov_b32_dpp v140, v146 row_shl:1 row_mask:0xf bank_mask:0xf bound_ctrl:1
	v_fma_f32 v141, -v199, v140, v132
	v_fmac_f32_e32 v146, v198, v140
	v_fmac_f32_e32 v146, v199, v133
	v_mov_b32_dpp v110, v141 row_shl:2 row_mask:0xf bank_mask:0xf bound_ctrl:1
	v_add_u32_e32 v132, 0x12660, v137
	v_mov_b32_dpp v111, v146 row_shl:2 row_mask:0xf bank_mask:0xf bound_ctrl:1
	s_nop 0
	s_waitcnt lgkmcnt(1)
	v_fmac_f32_e32 v141, v202, v110
	v_fma_f32 v140, -v203, v111, v141
	v_fmac_f32_e32 v146, v202, v111
	v_fmac_f32_e32 v146, v203, v110
	v_mov_b32_dpp v110, v140 row_shl:4 row_mask:0xf bank_mask:0xf bound_ctrl:1
	v_fmac_f32_e32 v140, v204, v110
	v_mov_b32_dpp v111, v146 row_shl:4 row_mask:0xf bank_mask:0xf bound_ctrl:1
	v_fma_f32 v124, -v205, v111, v140
	v_fmac_f32_e32 v146, v204, v111
	v_fmac_f32_e32 v146, v205, v110
	v_mov_b32_dpp v110, v124 row_shl:8 row_mask:0xf bank_mask:0xf bound_ctrl:1
	v_fmac_f32_e32 v124, v200, v110
	v_mov_b32_dpp v111, v146 row_shl:8 row_mask:0xf bank_mask:0xf bound_ctrl:1
	v_fma_f32 v147, -v201, v111, v124
	v_add_u32_e32 v124, 0x12640, v137
	v_add_u32_e32 v125, 0x12650, v137
	s_nop 0
	s_nop 0
	v_fmac_f32_e32 v146, v200, v111
	v_fmac_f32_e32 v146, v201, v110
	v_mov_b32_dpp v110, v147 row_shl:1 row_mask:0xf bank_mask:0xf bound_ctrl:1
	s_waitcnt lgkmcnt(0)
	v_fma_f32 v144, v212, v122, v106
	v_fma_f32 v144, -v213, v123, v144
	v_fma_f32 v145, v212, v123, v107
	v_mov_b32_dpp v111, v146 row_shl:1 row_mask:0xf bank_mask:0xf bound_ctrl:1
	v_fmac_f32_e32 v145, v213, v122
	v_fma_f32 v146, v212, v144, v98
	v_fma_f32 v146, -v213, v145, v146
	v_fma_f32 v145, v212, v145, v99
	v_fmac_f32_e32 v145, v213, v144
	v_fma_f32 v134, v212, v146, v134
	v_fma_f32 v134, -v213, v145, v134
	v_fmac_f32_e32 v135, v212, v145
	v_fmac_f32_e32 v135, v213, v146
	v_mov_b32_dpp v144, v134 row_shl:1 row_mask:0xf bank_mask:0xf bound_ctrl:1
	v_fmac_f32_e32 v134, v214, v144
	v_mov_b32_dpp v145, v135 row_shl:1 row_mask:0xf bank_mask:0xf bound_ctrl:1
	v_fma_f32 v134, -v215, v145, v134
	v_fmac_f32_e32 v135, v214, v145
	v_fmac_f32_e32 v135, v215, v144
	v_mov_b32_dpp v126, v134 row_shl:2 row_mask:0xf bank_mask:0xf bound_ctrl:1
	v_fmac_f32_e32 v134, v208, v126
	v_mov_b32_dpp v127, v135 row_shl:2 row_mask:0xf bank_mask:0xf bound_ctrl:1
	v_fma_f32 v134, -v209, v127, v134
	v_fmac_f32_e32 v135, v208, v127
	v_fmac_f32_e32 v135, v209, v126
	v_mov_b32_dpp v126, v134 row_shl:4 row_mask:0xf bank_mask:0xf bound_ctrl:1
	v_fmac_f32_e32 v134, v210, v126
	v_mov_b32_dpp v127, v135 row_shl:4 row_mask:0xf bank_mask:0xf bound_ctrl:1
	v_fma_f32 v134, -v211, v127, v134
	v_fmac_f32_e32 v135, v210, v127
	v_fmac_f32_e32 v135, v211, v126
	v_mov_b32_dpp v126, v134 row_shl:8 row_mask:0xf bank_mask:0xf bound_ctrl:1
	v_fmac_f32_e32 v134, v206, v126
	v_mov_b32_dpp v127, v135 row_shl:8 row_mask:0xf bank_mask:0xf bound_ctrl:1
	v_fma_f32 v134, -v207, v127, v134
	v_fmac_f32_e32 v135, v206, v127
	v_add_u32_e32 v127, 0x12820, v137
	v_fmac_f32_e32 v135, v207, v126
	v_add_u32_e32 v126, 0x12800, v137
	s_nop 0
	s_nop 0
	v_add_u32_e32 v132, 0x12810, v137
	v_mov_b32_dpp v126, v134 row_shl:1 row_mask:0xf bank_mask:0xf bound_ctrl:1
	v_mov_b32_dpp v127, v135 row_shl:1 row_mask:0xf bank_mask:0xf bound_ctrl:1
	s_nop 0
	s_waitcnt lgkmcnt(1)
	v_fma_f32 v144, v218, v116, v112
	v_fma_f32 v144, -v219, v117, v144
	v_fma_f32 v145, v218, v117, v113
	v_fmac_f32_e32 v145, v219, v116
	v_fma_f32 v148, v218, v144, v100
	v_fma_f32 v148, -v219, v145, v148
	v_fma_f32 v145, v218, v145, v101
	v_fmac_f32_e32 v145, v219, v144
	v_fma_f32 v128, v218, v148, v128
	v_fma_f32 v128, -v219, v145, v128
	v_fma_f32 v149, v218, v145, v129
	v_fmac_f32_e32 v149, v219, v148
	v_mov_b32_dpp v129, v128 row_shl:1 row_mask:0xf bank_mask:0xf bound_ctrl:1
	v_fmac_f32_e32 v128, v220, v129
	v_mov_b32_dpp v144, v149 row_shl:1 row_mask:0xf bank_mask:0xf bound_ctrl:1
	v_fma_f32 v145, -v221, v144, v128
	v_fmac_f32_e32 v149, v220, v144
	v_fmac_f32_e32 v149, v221, v129
	v_mov_b32_dpp v142, v145 row_shl:2 row_mask:0xf bank_mask:0xf bound_ctrl:1
	v_add_u32_e32 v128, 0x12860, v137
	v_mov_b32_dpp v143, v149 row_shl:2 row_mask:0xf bank_mask:0xf bound_ctrl:1
	s_nop 0
	s_waitcnt lgkmcnt(1)
	v_fmac_f32_e32 v145, v222, v142
	v_fma_f32 v144, -v223, v143, v145
	v_fmac_f32_e32 v149, v222, v143
	v_fmac_f32_e32 v149, v223, v142
	v_mov_b32_dpp v132, v144 row_shl:4 row_mask:0xf bank_mask:0xf bound_ctrl:1
	v_fmac_f32_e32 v144, v224, v132
	v_mov_b32_dpp v133, v149 row_shl:4 row_mask:0xf bank_mask:0xf bound_ctrl:1
	v_fma_f32 v142, -v225, v133, v144
	v_fmac_f32_e32 v149, v224, v133
	v_fmac_f32_e32 v149, v225, v132
	v_mov_b32_dpp v148, v142 row_shl:8 row_mask:0xf bank_mask:0xf bound_ctrl:1
	v_fmac_f32_e32 v142, v216, v148
	v_mov_b32_dpp v150, v149 row_shl:8 row_mask:0xf bank_mask:0xf bound_ctrl:1
	v_fma_f32 v151, -v217, v150, v142
	v_add_u32_e32 v142, 0x12840, v137
	v_add_u32_e32 v132, 0x12850, v137
	s_nop 0
	s_nop 0
	v_fmac_f32_e32 v149, v216, v150
	v_fmac_f32_e32 v149, v217, v148
	v_mov_b32_dpp v146, v151 row_shl:1 row_mask:0xf bank_mask:0xf bound_ctrl:1
	s_waitcnt lgkmcnt(0)
	v_fma_f32 v137, v232, v118, v114
	v_fma_f32 v137, -v233, v119, v137
	v_fma_f32 v148, v232, v119, v115
	v_mov_b32_dpp v147, v149 row_shl:1 row_mask:0xf bank_mask:0xf bound_ctrl:1
	v_fmac_f32_e32 v148, v233, v118
	v_fma_f32 v149, v232, v137, v102
	v_fma_f32 v149, -v233, v148, v149
	v_fma_f32 v148, v232, v148, v103
	v_fmac_f32_e32 v148, v233, v137
	v_fma_f32 v130, v232, v149, v130
	v_fmac_f32_e32 v131, v232, v148
	v_fma_f32 v130, -v233, v148, v130
	v_fmac_f32_e32 v131, v233, v149
	s_nop 0
	v_mov_b32_dpp v137, v130 row_shl:1 row_mask:0xf bank_mask:0xf bound_ctrl:1
	v_mov_b32_dpp v148, v131 row_shl:1 row_mask:0xf bank_mask:0xf bound_ctrl:1
	v_fmac_f32_e32 v130, v234, v137
	v_fmac_f32_e32 v131, v234, v148
	v_fma_f32 v130, -v235, v148, v130
	v_fmac_f32_e32 v131, v235, v137
	s_nop 0
	v_mov_b32_dpp v137, v130 row_shl:2 row_mask:0xf bank_mask:0xf bound_ctrl:1
	v_mov_b32_dpp v144, v131 row_shl:2 row_mask:0xf bank_mask:0xf bound_ctrl:1
	v_fmac_f32_e32 v130, v228, v137
	v_fmac_f32_e32 v131, v228, v144
	v_fma_f32 v130, -v229, v144, v130
	v_fmac_f32_e32 v131, v229, v137
	s_nop 0
	v_mov_b32_dpp v132, v130 row_shl:4 row_mask:0xf bank_mask:0xf bound_ctrl:1
	v_mov_b32_dpp v133, v131 row_shl:4 row_mask:0xf bank_mask:0xf bound_ctrl:1
	v_fmac_f32_e32 v130, v230, v132
	v_fmac_f32_e32 v131, v230, v133
	v_fma_f32 v130, -v231, v133, v130
	v_fmac_f32_e32 v131, v231, v132
	s_nop 0
	v_mov_b32_dpp v132, v130 row_shl:8 row_mask:0xf bank_mask:0xf bound_ctrl:1
	v_mov_b32_dpp v133, v131 row_shl:8 row_mask:0xf bank_mask:0xf bound_ctrl:1
	v_fmac_f32_e32 v130, v226, v132
	v_fmac_f32_e32 v131, v226, v133
	v_fma_f32 v130, -v227, v133, v130
	v_fmac_f32_e32 v131, v227, v132
	s_nop 0
	v_mov_b32_dpp v128, v130 row_shl:1 row_mask:0xf bank_mask:0xf bound_ctrl:1
	v_mov_b32_dpp v129, v131 row_shl:1 row_mask:0xf bank_mask:0xf bound_ctrl:1
	v_pk_fma_f32 v[130:131], v[196:197], v[110:111], v[120:121] op_sel_hi:[0,1,1]
	v_pk_fma_f32 v[116:117], v[218:219], v[146:147], v[116:117] op_sel_hi:[0,1,1]
	v_pk_fma_f32 v[118:119], v[232:233], v[128:129], v[118:119] op_sel_hi:[0,1,1]
	v_add_u32_e32 v121, s0, v189
	v_cvt_pk_f16_f32 v120, v110, v111
	v_pk_fma_f32 v[122:123], v[212:213], v[126:127], v[122:123] op_sel_hi:[0,1,1]
	v_pk_fma_f32 v[110:111], v[196:197], v[110:111], v[130:131] op_sel:[1,1,0] op_sel_hi:[1,0,1] neg_lo:[1,0,0]
	v_pk_fma_f32 v[130:131], v[218:219], v[146:147], v[116:117] op_sel:[1,1,0] op_sel_hi:[1,0,1] neg_lo:[1,0,0]
	v_pk_fma_f32 v[118:119], v[232:233], v[128:129], v[118:119] op_sel:[1,1,0] op_sel_hi:[1,0,1] neg_lo:[1,0,0]
	v_xor_b32_e32 v121, v121, v188
	v_pk_fma_f32 v[122:123], v[212:213], v[126:127], v[122:123] op_sel:[1,1,0] op_sel_hi:[1,0,1] neg_lo:[1,0,0]
	v_pk_fma_f32 v[116:117], v[196:197], v[110:111], v[104:105] op_sel_hi:[0,1,1]
	v_pk_fma_f32 v[112:113], v[218:219], v[130:131], v[112:113] op_sel_hi:[0,1,1]
	v_pk_fma_f32 v[114:115], v[232:233], v[118:119], v[114:115] op_sel_hi:[0,1,1]
	v_lshl_add_u32 v137, v121, 4, v190
	v_cvt_pk_f16_f32 v104, v110, v111
	v_pk_fma_f32 v[106:107], v[212:213], v[122:123], v[106:107] op_sel_hi:[0,1,1]
	v_pk_fma_f32 v[132:133], v[196:197], v[110:111], v[116:117] op_sel:[1,1,0] op_sel_hi:[1,0,1] neg_lo:[1,0,0]
	v_pk_fma_f32 v[134:135], v[218:219], v[130:131], v[112:113] op_sel:[1,1,0] op_sel_hi:[1,0,1] neg_lo:[1,0,0]
	v_pk_fma_f32 v[144:145], v[232:233], v[118:119], v[114:115] op_sel:[1,1,0] op_sel_hi:[1,0,1] neg_lo:[1,0,0]
	ds_read_b128 v[110:113], v137 offset:49152
	ds_read_b128 v[114:117], v137 offset:53248
	v_pk_fma_f32 v[106:107], v[212:213], v[122:123], v[106:107] op_sel:[1,1,0] op_sel_hi:[1,0,1] neg_lo:[1,0,0]
	v_pk_fma_f32 v[148:149], v[196:197], v[132:133], v[96:97] op_sel_hi:[0,1,1]
	v_pk_fma_f32 v[100:101], v[218:219], v[134:135], v[100:101] op_sel_hi:[0,1,1]
	v_pk_fma_f32 v[98:99], v[212:213], v[106:107], v[98:99] op_sel_hi:[0,1,1]
	v_pk_fma_f32 v[102:103], v[232:233], v[144:145], v[102:103] op_sel_hi:[0,1,1]
	v_cvt_pk_f16_f32 v96, v132, v133
	v_pk_fma_f32 v[108:109], v[196:197], v[132:133], v[148:149] op_sel:[1,1,0] op_sel_hi:[1,0,1] neg_lo:[1,0,0]
	v_pk_fma_f32 v[132:133], v[218:219], v[134:135], v[100:101] op_sel:[1,1,0] op_sel_hi:[1,0,1] neg_lo:[1,0,0]
	v_pk_fma_f32 v[98:99], v[212:213], v[106:107], v[98:99] op_sel:[1,1,0] op_sel_hi:[1,0,1] neg_lo:[1,0,0]
	v_pk_fma_f32 v[124:125], v[232:233], v[144:145], v[102:103] op_sel:[1,1,0] op_sel_hi:[1,0,1] neg_lo:[1,0,0]
	v_cvt_pk_f16_f32 v100, v108, v109
	v_cvt_pk_f16_f32 v102, v132, v133
	v_cvt_pk_f16_f32 v101, v98, v99
	v_cvt_pk_f16_f32 v103, v124, v125
	v_cvt_pk_f16_f32 v98, v134, v135
	v_cvt_pk_f16_f32 v97, v106, v107
	v_cvt_pk_f16_f32 v99, v144, v145
	v_cvt_pk_f16_f32 v106, v130, v131
	v_cvt_pk_f16_f32 v105, v122, v123
	v_cvt_pk_f16_f32 v107, v118, v119
	v_cvt_pk_f16_f32 v122, v146, v147
	v_cvt_pk_f16_f32 v121, v126, v127
	v_cvt_pk_f16_f32 v123, v128, v129
	s_waitcnt lgkmcnt(1)
	v_mfma_f32_16x16x32_f16 v[88:91], v[110:113], v[100:103], v[88:91]
	s_add_i32 s0, s0, 4
	v_add_u32_e32 v179, 0x400, v179
	v_add_u32_e32 v174, 0x1000, v174
	v_mfma_f32_16x16x32_f16 v[80:83], v[110:113], v[96:99], v[80:83]
	s_cmp_lg_u32 s0, 16
	v_add_u32_e32 v175, 0x1000, v175
	v_mfma_f32_16x16x32_f16 v[72:75], v[110:113], v[104:107], v[72:75]
	v_mfma_f32_16x16x32_f16 v[64:67], v[110:113], v[120:123], v[64:67]
	s_waitcnt lgkmcnt(0)
	v_mfma_f32_16x16x32_f16 v[56:59], v[114:117], v[100:103], v[56:59]
	v_mfma_f32_16x16x32_f16 v[48:51], v[114:117], v[96:99], v[48:51]
	v_mfma_f32_16x16x32_f16 v[40:43], v[114:117], v[104:107], v[40:43]
	v_mfma_f32_16x16x32_f16 v[32:35], v[114:117], v[120:123], v[32:35]
	ds_read_b128 v[108:111], v137 offset:57344
	ds_read_b128 v[112:115], v137 offset:61440
	s_waitcnt lgkmcnt(1)
	v_mfma_f32_16x16x32_f16 v[28:31], v[108:111], v[100:103], v[28:31]
	v_mfma_f32_16x16x32_f16 v[24:27], v[108:111], v[96:99], v[24:27]
	v_mfma_f32_16x16x32_f16 v[20:23], v[108:111], v[104:107], v[20:23]
	v_mfma_f32_16x16x32_f16 v[16:19], v[108:111], v[120:123], v[16:19]
	s_waitcnt lgkmcnt(0)
	v_mfma_f32_16x16x32_f16 v[12:15], v[112:115], v[100:103], v[12:15]
	v_mfma_f32_16x16x32_f16 v[8:11], v[112:115], v[96:99], v[8:11]
	v_mfma_f32_16x16x32_f16 v[4:7], v[112:115], v[104:107], v[4:7]
	v_mfma_f32_16x16x32_f16 v[0:3], v[112:115], v[120:123], v[0:3]
	s_cbranch_scc1 .LBB3_47
	s_ashr_i32 s45, s44, 31
	s_lshl_b64 s[0:1], s[44:45], 13
	v_lshl_add_u64 v[38:39], v[138:139], 0, s[0:1]
	s_mov_b32 s1, 0x3f3504f3
	v_mul_f32_e64 v36, |v88|, s1
	s_mov_b32 s3, 0x3ea7ba05
	v_fma_f32 v37, v36, s3, 1.0
	v_rcp_f32_e32 v44, v37
	v_mul_f32_e32 v37, 0xbfb8aa3b, v36
	v_mul_f32_e32 v36, v36, v37
	v_exp_f32_e32 v46, v36
	v_mul_f32_e64 v36, |v89|, s1
	v_fma_f32 v37, v36, s3, 1.0
	v_rcp_f32_e32 v45, v37
	v_mul_f32_e32 v37, 0xbfb8aa3b, v36
	v_mul_f32_e32 v36, v36, v37
	s_mov_b32 s2, 0xbfba00e3
	v_exp_f32_e32 v47, v36
	s_mov_b32 s0, 0x3f87dc22
	v_mov_b64_e32 v[36:37], s[2:3]
	v_pk_fma_f32 v[52:53], v[44:45], s[0:1], v[36:37] op_sel_hi:[1,0,0]
	s_mov_b32 s2, 0x3fb5f0e3
	v_pk_fma_f32 v[52:53], v[44:45], v[52:53], s[2:3] op_sel_hi:[1,1,0]
	s_mov_b32 s4, 0xbe91a98e
	v_pk_fma_f32 v[52:53], v[44:45], v[52:53], s[4:5] op_sel_hi:[1,1,0]
	s_mov_b32 s6, 0x3e827906
	v_pk_fma_f32 v[52:53], v[44:45], v[52:53], s[6:7] op_sel_hi:[1,1,0]
	v_cmp_le_f32_e32 vcc, 0, v89
	v_pk_mul_f32 v[44:45], v[44:45], v[52:53]
	v_mov_b32_e32 v137, 0
	v_pk_mul_f32 v[44:45], v[44:45], 0.5 op_sel_hi:[1,0]
	v_lshl_add_u64 v[38:39], v[38:39], 0, v[136:137]
	v_pk_mul_f32 v[44:45], v[46:47], v[44:45]
	s_nop 0
	v_pk_mul_f32 v[46:47], v[88:89], v[44:45]
	v_pk_fma_f32 v[44:45], v[88:89], v[44:45], v[88:89] neg_lo:[1,0,0] neg_hi:[1,0,0]
	s_nop 0
	v_cndmask_b32_e32 v45, v47, v45, vcc
	v_cmp_le_f32_e32 vcc, 0, v88
	s_nop 1
	v_cndmask_b32_e32 v44, v46, v44, vcc
	v_cvt_pk_f16_f32 v44, v44, v45
	v_mul_f32_e64 v45, |v90|, s1
	v_mul_f32_e32 v47, 0xbfb8aa3b, v45
	v_fma_f32 v46, v45, s3, 1.0
	v_mul_f32_e32 v45, v45, v47
	v_exp_f32_e32 v52, v45
	v_mul_f32_e64 v45, |v91|, s1
	v_fma_f32 v47, v45, s3, 1.0
	v_rcp_f32_e32 v46, v46
	v_rcp_f32_e32 v47, v47
	v_mul_f32_e32 v53, 0xbfb8aa3b, v45
	v_mul_f32_e32 v45, v45, v53
	v_exp_f32_e32 v53, v45
	v_pk_fma_f32 v[54:55], v[46:47], s[0:1], v[36:37] op_sel_hi:[1,0,0]
	v_cmp_le_f32_e32 vcc, 0, v91
	v_pk_fma_f32 v[54:55], v[46:47], v[54:55], s[2:3] op_sel_hi:[1,1,0]
	s_nop 0
	v_pk_fma_f32 v[54:55], v[46:47], v[54:55], s[4:5] op_sel_hi:[1,1,0]
	s_nop 0
	v_pk_fma_f32 v[54:55], v[46:47], v[54:55], s[6:7] op_sel_hi:[1,1,0]
	s_nop 0
	v_pk_mul_f32 v[46:47], v[46:47], v[54:55]
	s_nop 0
	v_pk_mul_f32 v[46:47], v[46:47], 0.5 op_sel_hi:[1,0]
	s_nop 0
	v_pk_mul_f32 v[46:47], v[52:53], v[46:47]
	s_nop 0
	v_pk_mul_f32 v[52:53], v[90:91], v[46:47]
	v_pk_fma_f32 v[46:47], v[90:91], v[46:47], v[90:91] neg_lo:[1,0,0] neg_hi:[1,0,0]
	s_nop 0
	v_cndmask_b32_e32 v45, v53, v47, vcc
	v_cmp_le_f32_e32 vcc, 0, v90
	v_mul_f32_e64 v47, |v81|, s1
	s_nop 0
	v_cndmask_b32_e32 v46, v52, v46, vcc
	v_cvt_pk_f16_f32 v45, v46, v45
	global_store_dwordx2 v[38:39], v[44:45], off
	v_mul_f32_e64 v45, |v80|, s1
	v_mul_f32_e32 v46, 0xbfb8aa3b, v45
	v_fma_f32 v44, v45, s3, 1.0
	v_mul_f32_e32 v45, v45, v46
	v_exp_f32_e32 v46, v45
	v_fma_f32 v45, v47, s3, 1.0
	v_rcp_f32_e32 v44, v44
	v_rcp_f32_e32 v45, v45
	v_mul_f32_e32 v52, 0xbfb8aa3b, v47
	v_mul_f32_e32 v47, v47, v52
	v_exp_f32_e32 v47, v47
	v_pk_fma_f32 v[52:53], v[44:45], s[0:1], v[36:37] op_sel_hi:[1,0,0]
	v_cmp_le_f32_e32 vcc, 0, v81
	v_pk_fma_f32 v[52:53], v[44:45], v[52:53], s[2:3] op_sel_hi:[1,1,0]
	s_nop 0
	v_pk_fma_f32 v[52:53], v[44:45], v[52:53], s[4:5] op_sel_hi:[1,1,0]
	s_nop 0
	v_pk_fma_f32 v[52:53], v[44:45], v[52:53], s[6:7] op_sel_hi:[1,1,0]
	s_nop 0
	v_pk_mul_f32 v[44:45], v[44:45], v[52:53]
	s_nop 0
	v_pk_mul_f32 v[44:45], v[44:45], 0.5 op_sel_hi:[1,0]
	s_nop 0
	v_pk_mul_f32 v[44:45], v[46:47], v[44:45]
	s_nop 0
	v_pk_mul_f32 v[46:47], v[80:81], v[44:45]
	v_pk_fma_f32 v[44:45], v[80:81], v[44:45], v[80:81] neg_lo:[1,0,0] neg_hi:[1,0,0]
	s_nop 0
	v_cndmask_b32_e32 v45, v47, v45, vcc
	v_cmp_le_f32_e32 vcc, 0, v80
	s_nop 1
	v_cndmask_b32_e32 v44, v46, v44, vcc
	v_cvt_pk_f16_f32 v44, v44, v45
	v_mul_f32_e64 v45, |v82|, s1
	v_mul_f32_e32 v47, 0xbfb8aa3b, v45
	v_fma_f32 v46, v45, s3, 1.0
	v_mul_f32_e32 v45, v45, v47
	v_exp_f32_e32 v52, v45
	v_mul_f32_e64 v45, |v83|, s1
	v_fma_f32 v47, v45, s3, 1.0
	v_rcp_f32_e32 v46, v46
	v_rcp_f32_e32 v47, v47
	v_mul_f32_e32 v53, 0xbfb8aa3b, v45
	v_mul_f32_e32 v45, v45, v53
	v_exp_f32_e32 v53, v45
	v_pk_fma_f32 v[54:55], v[46:47], s[0:1], v[36:37] op_sel_hi:[1,0,0]
	v_cmp_le_f32_e32 vcc, 0, v83
	v_pk_fma_f32 v[54:55], v[46:47], v[54:55], s[2:3] op_sel_hi:[1,1,0]
	s_nop 0
	v_pk_fma_f32 v[54:55], v[46:47], v[54:55], s[4:5] op_sel_hi:[1,1,0]
	s_nop 0
	v_pk_fma_f32 v[54:55], v[46:47], v[54:55], s[6:7] op_sel_hi:[1,1,0]
	s_nop 0
	v_pk_mul_f32 v[46:47], v[46:47], v[54:55]
	s_nop 0
	v_pk_mul_f32 v[46:47], v[46:47], 0.5 op_sel_hi:[1,0]
	s_nop 0
	v_pk_mul_f32 v[46:47], v[52:53], v[46:47]
	s_nop 0
	v_pk_mul_f32 v[52:53], v[82:83], v[46:47]
	v_pk_fma_f32 v[46:47], v[82:83], v[46:47], v[82:83] neg_lo:[1,0,0] neg_hi:[1,0,0]
	s_nop 0
	v_cndmask_b32_e32 v45, v53, v47, vcc
	v_cmp_le_f32_e32 vcc, 0, v82
	v_mul_f32_e64 v47, |v73|, s1
	s_nop 0
	v_cndmask_b32_e32 v46, v52, v46, vcc
	v_cvt_pk_f16_f32 v45, v46, v45
	global_store_dwordx2 v[38:39], v[44:45], off offset:128
	v_mul_f32_e64 v45, |v72|, s1
	v_mul_f32_e32 v46, 0xbfb8aa3b, v45
	v_fma_f32 v44, v45, s3, 1.0
	v_mul_f32_e32 v45, v45, v46
	v_exp_f32_e32 v46, v45
	v_fma_f32 v45, v47, s3, 1.0
	v_rcp_f32_e32 v44, v44
	v_rcp_f32_e32 v45, v45
	v_mul_f32_e32 v52, 0xbfb8aa3b, v47
	v_mul_f32_e32 v47, v47, v52
	v_exp_f32_e32 v47, v47
	v_pk_fma_f32 v[52:53], v[44:45], s[0:1], v[36:37] op_sel_hi:[1,0,0]
	v_cmp_le_f32_e32 vcc, 0, v73
	v_pk_fma_f32 v[52:53], v[44:45], v[52:53], s[2:3] op_sel_hi:[1,1,0]
	s_nop 0
	v_pk_fma_f32 v[52:53], v[44:45], v[52:53], s[4:5] op_sel_hi:[1,1,0]
	s_nop 0
	v_pk_fma_f32 v[52:53], v[44:45], v[52:53], s[6:7] op_sel_hi:[1,1,0]
	s_nop 0
	v_pk_mul_f32 v[44:45], v[44:45], v[52:53]
	s_nop 0
	v_pk_mul_f32 v[44:45], v[44:45], 0.5 op_sel_hi:[1,0]
	s_nop 0
	v_pk_mul_f32 v[44:45], v[46:47], v[44:45]
	s_nop 0
	v_pk_mul_f32 v[46:47], v[72:73], v[44:45]
	v_pk_fma_f32 v[44:45], v[72:73], v[44:45], v[72:73] neg_lo:[1,0,0] neg_hi:[1,0,0]
	s_nop 0
	v_cndmask_b32_e32 v45, v47, v45, vcc
	v_cmp_le_f32_e32 vcc, 0, v72
	s_nop 1
	v_cndmask_b32_e32 v44, v46, v44, vcc
	v_cvt_pk_f16_f32 v44, v44, v45
	v_mul_f32_e64 v45, |v74|, s1
	v_mul_f32_e32 v47, 0xbfb8aa3b, v45
	v_fma_f32 v46, v45, s3, 1.0
	v_mul_f32_e32 v45, v45, v47
	v_exp_f32_e32 v52, v45
	v_mul_f32_e64 v45, |v75|, s1
	v_fma_f32 v47, v45, s3, 1.0
	v_rcp_f32_e32 v46, v46
	v_rcp_f32_e32 v47, v47
	v_mul_f32_e32 v53, 0xbfb8aa3b, v45
	v_mul_f32_e32 v45, v45, v53
	v_exp_f32_e32 v53, v45
	v_pk_fma_f32 v[54:55], v[46:47], s[0:1], v[36:37] op_sel_hi:[1,0,0]
	v_cmp_le_f32_e32 vcc, 0, v75
	v_pk_fma_f32 v[54:55], v[46:47], v[54:55], s[2:3] op_sel_hi:[1,1,0]
	s_nop 0
	v_pk_fma_f32 v[54:55], v[46:47], v[54:55], s[4:5] op_sel_hi:[1,1,0]
	s_nop 0
	v_pk_fma_f32 v[54:55], v[46:47], v[54:55], s[6:7] op_sel_hi:[1,1,0]
	s_nop 0
	v_pk_mul_f32 v[46:47], v[46:47], v[54:55]
	s_nop 0
	v_pk_mul_f32 v[46:47], v[46:47], 0.5 op_sel_hi:[1,0]
	s_nop 0
	v_pk_mul_f32 v[46:47], v[52:53], v[46:47]
	s_nop 0
	v_pk_mul_f32 v[52:53], v[74:75], v[46:47]
	v_pk_fma_f32 v[46:47], v[74:75], v[46:47], v[74:75] neg_lo:[1,0,0] neg_hi:[1,0,0]
	s_nop 0
	v_cndmask_b32_e32 v45, v53, v47, vcc
	v_cmp_le_f32_e32 vcc, 0, v74
	v_mul_f32_e64 v47, |v65|, s1
	s_nop 0
	v_cndmask_b32_e32 v46, v52, v46, vcc
	v_cvt_pk_f16_f32 v45, v46, v45
	global_store_dwordx2 v[38:39], v[44:45], off offset:256
	v_mul_f32_e64 v45, |v64|, s1
	v_mul_f32_e32 v46, 0xbfb8aa3b, v45
	v_fma_f32 v44, v45, s3, 1.0
	v_mul_f32_e32 v45, v45, v46
	v_exp_f32_e32 v46, v45
	v_fma_f32 v45, v47, s3, 1.0
	v_rcp_f32_e32 v44, v44
	v_rcp_f32_e32 v45, v45
	v_mul_f32_e32 v52, 0xbfb8aa3b, v47
	v_mul_f32_e32 v47, v47, v52
	v_exp_f32_e32 v47, v47
	v_pk_fma_f32 v[52:53], v[44:45], s[0:1], v[36:37] op_sel_hi:[1,0,0]
	v_cmp_le_f32_e32 vcc, 0, v65
	v_pk_fma_f32 v[52:53], v[44:45], v[52:53], s[2:3] op_sel_hi:[1,1,0]
	s_nop 0
	v_pk_fma_f32 v[52:53], v[44:45], v[52:53], s[4:5] op_sel_hi:[1,1,0]
	s_nop 0
	v_pk_fma_f32 v[52:53], v[44:45], v[52:53], s[6:7] op_sel_hi:[1,1,0]
	s_nop 0
	v_pk_mul_f32 v[44:45], v[44:45], v[52:53]
	s_nop 0
	v_pk_mul_f32 v[44:45], v[44:45], 0.5 op_sel_hi:[1,0]
	s_nop 0
	v_pk_mul_f32 v[44:45], v[46:47], v[44:45]
	s_nop 0
	v_pk_mul_f32 v[46:47], v[64:65], v[44:45]
	v_pk_fma_f32 v[44:45], v[64:65], v[44:45], v[64:65] neg_lo:[1,0,0] neg_hi:[1,0,0]
	s_nop 0
	v_cndmask_b32_e32 v45, v47, v45, vcc
	v_cmp_le_f32_e32 vcc, 0, v64
	s_nop 1
	v_cndmask_b32_e32 v44, v46, v44, vcc
	v_cvt_pk_f16_f32 v44, v44, v45
	v_mul_f32_e64 v45, |v66|, s1
	v_mul_f32_e32 v47, 0xbfb8aa3b, v45
	v_fma_f32 v46, v45, s3, 1.0
	v_mul_f32_e32 v45, v45, v47
	v_exp_f32_e32 v52, v45
	v_mul_f32_e64 v45, |v67|, s1
	v_fma_f32 v47, v45, s3, 1.0
	v_rcp_f32_e32 v46, v46
	v_rcp_f32_e32 v47, v47
	v_mul_f32_e32 v53, 0xbfb8aa3b, v45
	v_mul_f32_e32 v45, v45, v53
	v_exp_f32_e32 v53, v45
	v_pk_fma_f32 v[54:55], v[46:47], s[0:1], v[36:37] op_sel_hi:[1,0,0]
	v_cmp_le_f32_e32 vcc, 0, v67
	v_pk_fma_f32 v[54:55], v[46:47], v[54:55], s[2:3] op_sel_hi:[1,1,0]
	s_nop 0
	v_pk_fma_f32 v[54:55], v[46:47], v[54:55], s[4:5] op_sel_hi:[1,1,0]
	s_nop 0
	v_pk_fma_f32 v[54:55], v[46:47], v[54:55], s[6:7] op_sel_hi:[1,1,0]
	s_nop 0
	v_pk_mul_f32 v[46:47], v[46:47], v[54:55]
	s_nop 0
	v_pk_mul_f32 v[46:47], v[46:47], 0.5 op_sel_hi:[1,0]
	s_nop 0
	v_pk_mul_f32 v[46:47], v[52:53], v[46:47]
	s_nop 0
	v_pk_mul_f32 v[52:53], v[66:67], v[46:47]
	v_pk_fma_f32 v[46:47], v[66:67], v[46:47], v[66:67] neg_lo:[1,0,0] neg_hi:[1,0,0]
	s_nop 0
	v_cndmask_b32_e32 v45, v53, v47, vcc
	v_cmp_le_f32_e32 vcc, 0, v66
	v_mul_f32_e64 v47, |v57|, s1
	s_nop 0
	v_cndmask_b32_e32 v46, v52, v46, vcc
	v_cvt_pk_f16_f32 v45, v46, v45
	global_store_dwordx2 v[38:39], v[44:45], off offset:384
	v_mul_f32_e64 v45, |v56|, s1
	v_mul_f32_e32 v46, 0xbfb8aa3b, v45
	v_fma_f32 v44, v45, s3, 1.0
	v_mul_f32_e32 v45, v45, v46
	v_exp_f32_e32 v46, v45
	v_fma_f32 v45, v47, s3, 1.0
	v_rcp_f32_e32 v44, v44
	v_rcp_f32_e32 v45, v45
	v_mul_f32_e32 v52, 0xbfb8aa3b, v47
	v_mul_f32_e32 v47, v47, v52
	v_exp_f32_e32 v47, v47
	v_pk_fma_f32 v[52:53], v[44:45], s[0:1], v[36:37] op_sel_hi:[1,0,0]
	v_cmp_le_f32_e32 vcc, 0, v57
	v_pk_fma_f32 v[52:53], v[44:45], v[52:53], s[2:3] op_sel_hi:[1,1,0]
	s_nop 0
	v_pk_fma_f32 v[52:53], v[44:45], v[52:53], s[4:5] op_sel_hi:[1,1,0]
	s_nop 0
	v_pk_fma_f32 v[52:53], v[44:45], v[52:53], s[6:7] op_sel_hi:[1,1,0]
	s_nop 0
	v_pk_mul_f32 v[44:45], v[44:45], v[52:53]
	s_nop 0
	v_pk_mul_f32 v[44:45], v[44:45], 0.5 op_sel_hi:[1,0]
	s_nop 0
	v_pk_mul_f32 v[44:45], v[46:47], v[44:45]
	s_nop 0
	v_pk_mul_f32 v[46:47], v[56:57], v[44:45]
	v_pk_fma_f32 v[44:45], v[56:57], v[44:45], v[56:57] neg_lo:[1,0,0] neg_hi:[1,0,0]
	s_nop 0
	v_cndmask_b32_e32 v45, v47, v45, vcc
	v_cmp_le_f32_e32 vcc, 0, v56
	s_nop 1
	v_cndmask_b32_e32 v44, v46, v44, vcc
	v_cvt_pk_f16_f32 v44, v44, v45
	v_mul_f32_e64 v45, |v58|, s1
	v_mul_f32_e32 v47, 0xbfb8aa3b, v45
	v_fma_f32 v46, v45, s3, 1.0
	v_mul_f32_e32 v45, v45, v47
	v_exp_f32_e32 v52, v45
	v_mul_f32_e64 v45, |v59|, s1
	v_fma_f32 v47, v45, s3, 1.0
	v_rcp_f32_e32 v46, v46
	v_rcp_f32_e32 v47, v47
	v_mul_f32_e32 v53, 0xbfb8aa3b, v45
	v_mul_f32_e32 v45, v45, v53
	v_exp_f32_e32 v53, v45
	v_pk_fma_f32 v[54:55], v[46:47], s[0:1], v[36:37] op_sel_hi:[1,0,0]
	v_cmp_le_f32_e32 vcc, 0, v59
	v_pk_fma_f32 v[54:55], v[46:47], v[54:55], s[2:3] op_sel_hi:[1,1,0]
	s_nop 0
	v_pk_fma_f32 v[54:55], v[46:47], v[54:55], s[4:5] op_sel_hi:[1,1,0]
	s_nop 0
	v_pk_fma_f32 v[54:55], v[46:47], v[54:55], s[6:7] op_sel_hi:[1,1,0]
	s_nop 0
	v_pk_mul_f32 v[46:47], v[46:47], v[54:55]
	s_nop 0
	v_pk_mul_f32 v[46:47], v[46:47], 0.5 op_sel_hi:[1,0]
	s_nop 0
	v_pk_mul_f32 v[46:47], v[52:53], v[46:47]
	s_nop 0
	v_pk_mul_f32 v[52:53], v[58:59], v[46:47]
	v_pk_fma_f32 v[46:47], v[58:59], v[46:47], v[58:59] neg_lo:[1,0,0] neg_hi:[1,0,0]
	s_nop 0
	v_cndmask_b32_e32 v45, v53, v47, vcc
	v_cmp_le_f32_e32 vcc, 0, v58
	v_mul_f32_e64 v47, |v49|, s1
	s_nop 0
	v_cndmask_b32_e32 v46, v52, v46, vcc
	v_cvt_pk_f16_f32 v45, v46, v45
	global_store_dwordx2 v[38:39], v[44:45], off offset:32
	v_mul_f32_e64 v45, |v48|, s1
	v_mul_f32_e32 v46, 0xbfb8aa3b, v45
	v_fma_f32 v44, v45, s3, 1.0
	v_mul_f32_e32 v45, v45, v46
	v_exp_f32_e32 v46, v45
	v_fma_f32 v45, v47, s3, 1.0
	v_rcp_f32_e32 v44, v44
	v_rcp_f32_e32 v45, v45
	v_mul_f32_e32 v52, 0xbfb8aa3b, v47
	v_mul_f32_e32 v47, v47, v52
	v_exp_f32_e32 v47, v47
	v_pk_fma_f32 v[52:53], v[44:45], s[0:1], v[36:37] op_sel_hi:[1,0,0]
	v_cmp_le_f32_e32 vcc, 0, v49
	v_pk_fma_f32 v[52:53], v[44:45], v[52:53], s[2:3] op_sel_hi:[1,1,0]
	s_nop 0
	v_pk_fma_f32 v[52:53], v[44:45], v[52:53], s[4:5] op_sel_hi:[1,1,0]
	s_nop 0
	v_pk_fma_f32 v[52:53], v[44:45], v[52:53], s[6:7] op_sel_hi:[1,1,0]
	s_nop 0
	v_pk_mul_f32 v[44:45], v[44:45], v[52:53]
	s_nop 0
	v_pk_mul_f32 v[44:45], v[44:45], 0.5 op_sel_hi:[1,0]
	s_nop 0
	v_pk_mul_f32 v[44:45], v[46:47], v[44:45]
	s_nop 0
	v_pk_mul_f32 v[46:47], v[48:49], v[44:45]
	v_pk_fma_f32 v[44:45], v[48:49], v[44:45], v[48:49] neg_lo:[1,0,0] neg_hi:[1,0,0]
	s_nop 0
	v_cndmask_b32_e32 v45, v47, v45, vcc
	v_cmp_le_f32_e32 vcc, 0, v48
	s_nop 1
	v_cndmask_b32_e32 v44, v46, v44, vcc
	v_cvt_pk_f16_f32 v44, v44, v45
	v_mul_f32_e64 v45, |v50|, s1
	v_mul_f32_e32 v47, 0xbfb8aa3b, v45
	v_fma_f32 v46, v45, s3, 1.0
	v_mul_f32_e32 v45, v45, v47
	v_exp_f32_e32 v48, v45
	v_mul_f32_e64 v45, |v51|, s1
	v_fma_f32 v47, v45, s3, 1.0
	v_rcp_f32_e32 v46, v46
	v_rcp_f32_e32 v47, v47
	v_mul_f32_e32 v49, 0xbfb8aa3b, v45
	v_mul_f32_e32 v45, v45, v49
	v_exp_f32_e32 v49, v45
	v_pk_fma_f32 v[52:53], v[46:47], s[0:1], v[36:37] op_sel_hi:[1,0,0]
	v_cmp_le_f32_e32 vcc, 0, v51
	v_pk_fma_f32 v[52:53], v[46:47], v[52:53], s[2:3] op_sel_hi:[1,1,0]
	s_nop 0
	v_pk_fma_f32 v[52:53], v[46:47], v[52:53], s[4:5] op_sel_hi:[1,1,0]
	s_nop 0
	v_pk_fma_f32 v[52:53], v[46:47], v[52:53], s[6:7] op_sel_hi:[1,1,0]
	s_nop 0
	v_pk_mul_f32 v[46:47], v[46:47], v[52:53]
	s_nop 0
	v_pk_mul_f32 v[46:47], v[46:47], 0.5 op_sel_hi:[1,0]
	s_nop 0
	v_pk_mul_f32 v[46:47], v[48:49], v[46:47]
	s_nop 0
	v_pk_mul_f32 v[48:49], v[50:51], v[46:47]
	v_pk_fma_f32 v[46:47], v[50:51], v[46:47], v[50:51] neg_lo:[1,0,0] neg_hi:[1,0,0]
	s_nop 0
	v_cndmask_b32_e32 v45, v49, v47, vcc
	v_cmp_le_f32_e32 vcc, 0, v50
	v_mul_f32_e64 v47, |v41|, s1
	s_nop 0
	v_cndmask_b32_e32 v46, v48, v46, vcc
	v_cvt_pk_f16_f32 v45, v46, v45
	global_store_dwordx2 v[38:39], v[44:45], off offset:160
	v_mul_f32_e64 v45, |v40|, s1
	v_mul_f32_e32 v46, 0xbfb8aa3b, v45
	v_fma_f32 v44, v45, s3, 1.0
	v_mul_f32_e32 v45, v45, v46
	v_exp_f32_e32 v46, v45
	v_fma_f32 v45, v47, s3, 1.0
	v_rcp_f32_e32 v44, v44
	v_rcp_f32_e32 v45, v45
	v_mul_f32_e32 v48, 0xbfb8aa3b, v47
	v_mul_f32_e32 v47, v47, v48
	v_exp_f32_e32 v47, v47
	v_pk_fma_f32 v[48:49], v[44:45], s[0:1], v[36:37] op_sel_hi:[1,0,0]
	v_cmp_le_f32_e32 vcc, 0, v41
	v_pk_fma_f32 v[48:49], v[44:45], v[48:49], s[2:3] op_sel_hi:[1,1,0]
	s_nop 0
	v_pk_fma_f32 v[48:49], v[44:45], v[48:49], s[4:5] op_sel_hi:[1,1,0]
	s_nop 0
	v_pk_fma_f32 v[48:49], v[44:45], v[48:49], s[6:7] op_sel_hi:[1,1,0]
	s_nop 0
	v_pk_mul_f32 v[44:45], v[44:45], v[48:49]
	s_nop 0
	v_pk_mul_f32 v[44:45], v[44:45], 0.5 op_sel_hi:[1,0]
	s_nop 0
	v_pk_mul_f32 v[44:45], v[46:47], v[44:45]
	s_nop 0
	v_pk_mul_f32 v[46:47], v[40:41], v[44:45]
	v_pk_fma_f32 v[44:45], v[40:41], v[44:45], v[40:41] neg_lo:[1,0,0] neg_hi:[1,0,0]
	s_nop 0
	v_cndmask_b32_e32 v41, v47, v45, vcc
	v_cmp_le_f32_e32 vcc, 0, v40
	s_nop 1
	v_cndmask_b32_e32 v40, v46, v44, vcc
	v_cvt_pk_f16_f32 v40, v40, v41
	v_mul_f32_e64 v41, |v42|, s1
	v_mul_f32_e32 v45, 0xbfb8aa3b, v41
	v_fma_f32 v44, v41, s3, 1.0
	v_mul_f32_e32 v41, v41, v45
	v_exp_f32_e32 v46, v41
	v_mul_f32_e64 v41, |v43|, s1
	v_fma_f32 v45, v41, s3, 1.0
	v_rcp_f32_e32 v44, v44
	v_rcp_f32_e32 v45, v45
	v_mul_f32_e32 v47, 0xbfb8aa3b, v41
	v_mul_f32_e32 v41, v41, v47
	v_exp_f32_e32 v47, v41
	v_pk_fma_f32 v[48:49], v[44:45], s[0:1], v[36:37] op_sel_hi:[1,0,0]
	v_cmp_le_f32_e32 vcc, 0, v43
	v_pk_fma_f32 v[48:49], v[44:45], v[48:49], s[2:3] op_sel_hi:[1,1,0]
	s_nop 0
	v_pk_fma_f32 v[48:49], v[44:45], v[48:49], s[4:5] op_sel_hi:[1,1,0]
	s_nop 0
	v_pk_fma_f32 v[48:49], v[44:45], v[48:49], s[6:7] op_sel_hi:[1,1,0]
	s_nop 0
	v_pk_mul_f32 v[44:45], v[44:45], v[48:49]
	s_nop 0
	v_pk_mul_f32 v[44:45], v[44:45], 0.5 op_sel_hi:[1,0]
	s_nop 0
	v_pk_mul_f32 v[44:45], v[46:47], v[44:45]
	s_nop 0
	v_pk_mul_f32 v[46:47], v[42:43], v[44:45]
	v_pk_fma_f32 v[44:45], v[42:43], v[44:45], v[42:43] neg_lo:[1,0,0] neg_hi:[1,0,0]
	v_mul_f32_e64 v43, |v33|, s1
	v_cndmask_b32_e32 v41, v47, v45, vcc
	v_cmp_le_f32_e32 vcc, 0, v42
	s_nop 1
	v_cndmask_b32_e32 v42, v46, v44, vcc
	v_cvt_pk_f16_f32 v41, v42, v41
	global_store_dwordx2 v[38:39], v[40:41], off offset:288
	v_mul_f32_e64 v41, |v32|, s1
	v_mul_f32_e32 v42, 0xbfb8aa3b, v41
	v_fma_f32 v40, v41, s3, 1.0
	v_mul_f32_e32 v41, v41, v42
	v_exp_f32_e32 v42, v41
	v_fma_f32 v41, v43, s3, 1.0
	v_rcp_f32_e32 v40, v40
	v_rcp_f32_e32 v41, v41
	v_mul_f32_e32 v44, 0xbfb8aa3b, v43
	v_mul_f32_e32 v43, v43, v44
	v_exp_f32_e32 v43, v43
	v_pk_fma_f32 v[44:45], v[40:41], s[0:1], v[36:37] op_sel_hi:[1,0,0]
	v_cmp_le_f32_e32 vcc, 0, v33
	v_pk_fma_f32 v[44:45], v[40:41], v[44:45], s[2:3] op_sel_hi:[1,1,0]
	s_nop 0
	v_pk_fma_f32 v[44:45], v[40:41], v[44:45], s[4:5] op_sel_hi:[1,1,0]
	s_nop 0
	v_pk_fma_f32 v[44:45], v[40:41], v[44:45], s[6:7] op_sel_hi:[1,1,0]
	s_nop 0
	v_pk_mul_f32 v[40:41], v[40:41], v[44:45]
	s_nop 0
	v_pk_mul_f32 v[40:41], v[40:41], 0.5 op_sel_hi:[1,0]
	s_nop 0
	v_pk_mul_f32 v[40:41], v[42:43], v[40:41]
	s_nop 0
	v_pk_mul_f32 v[42:43], v[32:33], v[40:41]
	v_pk_fma_f32 v[40:41], v[32:33], v[40:41], v[32:33] neg_lo:[1,0,0] neg_hi:[1,0,0]
	s_nop 0
	v_cndmask_b32_e32 v33, v43, v41, vcc
	v_cmp_le_f32_e32 vcc, 0, v32
	s_nop 1
	v_cndmask_b32_e32 v32, v42, v40, vcc
	v_cvt_pk_f16_f32 v32, v32, v33
	v_mul_f32_e64 v33, |v34|, s1
	v_mul_f32_e32 v41, 0xbfb8aa3b, v33
	v_fma_f32 v40, v33, s3, 1.0
	v_mul_f32_e32 v33, v33, v41
	v_exp_f32_e32 v42, v33
	v_mul_f32_e64 v33, |v35|, s1
	v_fma_f32 v41, v33, s3, 1.0
	v_rcp_f32_e32 v40, v40
	v_rcp_f32_e32 v41, v41
	v_mul_f32_e32 v43, 0xbfb8aa3b, v33
	v_mul_f32_e32 v33, v33, v43
	v_exp_f32_e32 v43, v33
	v_pk_fma_f32 v[44:45], v[40:41], s[0:1], v[36:37] op_sel_hi:[1,0,0]
	v_cmp_le_f32_e32 vcc, 0, v35
	v_pk_fma_f32 v[44:45], v[40:41], v[44:45], s[2:3] op_sel_hi:[1,1,0]
	s_nop 0
	v_pk_fma_f32 v[44:45], v[40:41], v[44:45], s[4:5] op_sel_hi:[1,1,0]
	s_nop 0
	v_pk_fma_f32 v[44:45], v[40:41], v[44:45], s[6:7] op_sel_hi:[1,1,0]
	s_nop 0
	v_pk_mul_f32 v[40:41], v[40:41], v[44:45]
	s_nop 0
	v_pk_mul_f32 v[40:41], v[40:41], 0.5 op_sel_hi:[1,0]
	s_nop 0
	v_pk_mul_f32 v[40:41], v[42:43], v[40:41]
	s_nop 0
	v_pk_mul_f32 v[42:43], v[34:35], v[40:41]
	v_pk_fma_f32 v[40:41], v[34:35], v[40:41], v[34:35] neg_lo:[1,0,0] neg_hi:[1,0,0]
	v_mul_f32_e64 v35, |v29|, s1
	v_cndmask_b32_e32 v33, v43, v41, vcc
	v_cmp_le_f32_e32 vcc, 0, v34
	s_nop 1
	v_cndmask_b32_e32 v34, v42, v40, vcc
	v_cvt_pk_f16_f32 v33, v34, v33
	global_store_dwordx2 v[38:39], v[32:33], off offset:416
	v_mul_f32_e64 v33, |v28|, s1
	v_mul_f32_e32 v34, 0xbfb8aa3b, v33
	v_fma_f32 v32, v33, s3, 1.0
	v_mul_f32_e32 v33, v33, v34
	v_exp_f32_e32 v34, v33
	v_fma_f32 v33, v35, s3, 1.0
	v_rcp_f32_e32 v32, v32
	v_rcp_f32_e32 v33, v33
	v_mul_f32_e32 v40, 0xbfb8aa3b, v35
	v_mul_f32_e32 v35, v35, v40
	v_exp_f32_e32 v35, v35
	v_pk_fma_f32 v[40:41], v[32:33], s[0:1], v[36:37] op_sel_hi:[1,0,0]
	v_cmp_le_f32_e32 vcc, 0, v29
	v_pk_fma_f32 v[40:41], v[32:33], v[40:41], s[2:3] op_sel_hi:[1,1,0]
	s_nop 0
	v_pk_fma_f32 v[40:41], v[32:33], v[40:41], s[4:5] op_sel_hi:[1,1,0]
	s_nop 0
	v_pk_fma_f32 v[40:41], v[32:33], v[40:41], s[6:7] op_sel_hi:[1,1,0]
	s_nop 0
	v_pk_mul_f32 v[32:33], v[32:33], v[40:41]
	s_nop 0
	v_pk_mul_f32 v[32:33], v[32:33], 0.5 op_sel_hi:[1,0]
	s_nop 0
	v_pk_mul_f32 v[32:33], v[34:35], v[32:33]
	s_nop 0
	v_pk_mul_f32 v[34:35], v[28:29], v[32:33]
	v_pk_fma_f32 v[32:33], v[28:29], v[32:33], v[28:29] neg_lo:[1,0,0] neg_hi:[1,0,0]
	s_nop 0
	v_cndmask_b32_e32 v29, v35, v33, vcc
	v_cmp_le_f32_e32 vcc, 0, v28
	s_nop 1
	v_cndmask_b32_e32 v28, v34, v32, vcc
	v_cvt_pk_f16_f32 v28, v28, v29
	v_mul_f32_e64 v29, |v30|, s1
	v_mul_f32_e32 v33, 0xbfb8aa3b, v29
	v_fma_f32 v32, v29, s3, 1.0
	v_mul_f32_e32 v29, v29, v33
	v_exp_f32_e32 v34, v29
	v_mul_f32_e64 v29, |v31|, s1
	v_fma_f32 v33, v29, s3, 1.0
	v_rcp_f32_e32 v32, v32
	v_rcp_f32_e32 v33, v33
	v_mul_f32_e32 v35, 0xbfb8aa3b, v29
	v_mul_f32_e32 v29, v29, v35
	v_exp_f32_e32 v35, v29
	v_pk_fma_f32 v[40:41], v[32:33], s[0:1], v[36:37] op_sel_hi:[1,0,0]
	v_cmp_le_f32_e32 vcc, 0, v31
	v_pk_fma_f32 v[40:41], v[32:33], v[40:41], s[2:3] op_sel_hi:[1,1,0]
	s_nop 0
	v_pk_fma_f32 v[40:41], v[32:33], v[40:41], s[4:5] op_sel_hi:[1,1,0]
	s_nop 0
	v_pk_fma_f32 v[40:41], v[32:33], v[40:41], s[6:7] op_sel_hi:[1,1,0]
	s_nop 0
	v_pk_mul_f32 v[32:33], v[32:33], v[40:41]
	s_nop 0
	v_pk_mul_f32 v[32:33], v[32:33], 0.5 op_sel_hi:[1,0]
	s_nop 0
	v_pk_mul_f32 v[32:33], v[34:35], v[32:33]
	s_nop 0
	v_pk_mul_f32 v[34:35], v[30:31], v[32:33]
	v_pk_fma_f32 v[32:33], v[30:31], v[32:33], v[30:31] neg_lo:[1,0,0] neg_hi:[1,0,0]
	v_mul_f32_e64 v31, |v25|, s1
	v_cndmask_b32_e32 v29, v35, v33, vcc
	v_cmp_le_f32_e32 vcc, 0, v30
	s_nop 1
	v_cndmask_b32_e32 v30, v34, v32, vcc
	v_cvt_pk_f16_f32 v29, v30, v29
	global_store_dwordx2 v[38:39], v[28:29], off offset:64
	v_mul_f32_e64 v29, |v24|, s1
	v_mul_f32_e32 v30, 0xbfb8aa3b, v29
	v_fma_f32 v28, v29, s3, 1.0
	v_mul_f32_e32 v29, v29, v30
	v_exp_f32_e32 v30, v29
	v_fma_f32 v29, v31, s3, 1.0
	v_rcp_f32_e32 v28, v28
	v_rcp_f32_e32 v29, v29
	v_mul_f32_e32 v32, 0xbfb8aa3b, v31
	v_mul_f32_e32 v31, v31, v32
	v_exp_f32_e32 v31, v31
	v_pk_fma_f32 v[32:33], v[28:29], s[0:1], v[36:37] op_sel_hi:[1,0,0]
	v_cmp_le_f32_e32 vcc, 0, v25
	v_pk_fma_f32 v[32:33], v[28:29], v[32:33], s[2:3] op_sel_hi:[1,1,0]
	s_nop 0
	v_pk_fma_f32 v[32:33], v[28:29], v[32:33], s[4:5] op_sel_hi:[1,1,0]
	s_nop 0
	v_pk_fma_f32 v[32:33], v[28:29], v[32:33], s[6:7] op_sel_hi:[1,1,0]
	s_nop 0
	v_pk_mul_f32 v[28:29], v[28:29], v[32:33]
	s_nop 0
	v_pk_mul_f32 v[28:29], v[28:29], 0.5 op_sel_hi:[1,0]
	s_nop 0
	v_pk_mul_f32 v[28:29], v[30:31], v[28:29]
	s_nop 0
	v_pk_mul_f32 v[30:31], v[24:25], v[28:29]
	v_pk_fma_f32 v[28:29], v[24:25], v[28:29], v[24:25] neg_lo:[1,0,0] neg_hi:[1,0,0]
	s_nop 0
	v_cndmask_b32_e32 v25, v31, v29, vcc
	v_cmp_le_f32_e32 vcc, 0, v24
	s_nop 1
	v_cndmask_b32_e32 v24, v30, v28, vcc
	v_cvt_pk_f16_f32 v24, v24, v25
	v_mul_f32_e64 v25, |v26|, s1
	v_mul_f32_e32 v29, 0xbfb8aa3b, v25
	v_fma_f32 v28, v25, s3, 1.0
	v_mul_f32_e32 v25, v25, v29
	v_exp_f32_e32 v30, v25
	v_mul_f32_e64 v25, |v27|, s1
	v_fma_f32 v29, v25, s3, 1.0
	v_rcp_f32_e32 v28, v28
	v_rcp_f32_e32 v29, v29
	v_mul_f32_e32 v31, 0xbfb8aa3b, v25
	v_mul_f32_e32 v25, v25, v31
	v_exp_f32_e32 v31, v25
	v_pk_fma_f32 v[32:33], v[28:29], s[0:1], v[36:37] op_sel_hi:[1,0,0]
	v_cmp_le_f32_e32 vcc, 0, v27
	v_pk_fma_f32 v[32:33], v[28:29], v[32:33], s[2:3] op_sel_hi:[1,1,0]
	s_nop 0
	v_pk_fma_f32 v[32:33], v[28:29], v[32:33], s[4:5] op_sel_hi:[1,1,0]
	s_nop 0
	v_pk_fma_f32 v[32:33], v[28:29], v[32:33], s[6:7] op_sel_hi:[1,1,0]
	s_nop 0
	v_pk_mul_f32 v[28:29], v[28:29], v[32:33]
	s_nop 0
	v_pk_mul_f32 v[28:29], v[28:29], 0.5 op_sel_hi:[1,0]
	s_nop 0
	v_pk_mul_f32 v[28:29], v[30:31], v[28:29]
	s_nop 0
	v_pk_mul_f32 v[30:31], v[26:27], v[28:29]
	v_pk_fma_f32 v[28:29], v[26:27], v[28:29], v[26:27] neg_lo:[1,0,0] neg_hi:[1,0,0]
	v_mul_f32_e64 v27, |v21|, s1
	v_cndmask_b32_e32 v25, v31, v29, vcc
	v_cmp_le_f32_e32 vcc, 0, v26
	s_nop 1
	v_cndmask_b32_e32 v26, v30, v28, vcc
	v_cvt_pk_f16_f32 v25, v26, v25
	global_store_dwordx2 v[38:39], v[24:25], off offset:192
	v_mul_f32_e64 v25, |v20|, s1
	v_mul_f32_e32 v26, 0xbfb8aa3b, v25
	v_fma_f32 v24, v25, s3, 1.0
	v_mul_f32_e32 v25, v25, v26
	v_exp_f32_e32 v26, v25
	v_fma_f32 v25, v27, s3, 1.0
	v_rcp_f32_e32 v24, v24
	v_rcp_f32_e32 v25, v25
	v_mul_f32_e32 v28, 0xbfb8aa3b, v27
	v_mul_f32_e32 v27, v27, v28
	v_exp_f32_e32 v27, v27
	v_pk_fma_f32 v[28:29], v[24:25], s[0:1], v[36:37] op_sel_hi:[1,0,0]
	v_cmp_le_f32_e32 vcc, 0, v21
	v_pk_fma_f32 v[28:29], v[24:25], v[28:29], s[2:3] op_sel_hi:[1,1,0]
	s_nop 0
	v_pk_fma_f32 v[28:29], v[24:25], v[28:29], s[4:5] op_sel_hi:[1,1,0]
	s_nop 0
	v_pk_fma_f32 v[28:29], v[24:25], v[28:29], s[6:7] op_sel_hi:[1,1,0]
	s_nop 0
	v_pk_mul_f32 v[24:25], v[24:25], v[28:29]
	s_nop 0
	v_pk_mul_f32 v[24:25], v[24:25], 0.5 op_sel_hi:[1,0]
	s_nop 0
	v_pk_mul_f32 v[24:25], v[26:27], v[24:25]
	s_nop 0
	v_pk_mul_f32 v[26:27], v[20:21], v[24:25]
	v_pk_fma_f32 v[24:25], v[20:21], v[24:25], v[20:21] neg_lo:[1,0,0] neg_hi:[1,0,0]
	s_nop 0
	v_cndmask_b32_e32 v21, v27, v25, vcc
	v_cmp_le_f32_e32 vcc, 0, v20
	s_nop 1
	v_cndmask_b32_e32 v20, v26, v24, vcc
	v_cvt_pk_f16_f32 v20, v20, v21
	v_mul_f32_e64 v21, |v22|, s1
	v_mul_f32_e32 v25, 0xbfb8aa3b, v21
	v_fma_f32 v24, v21, s3, 1.0
	v_mul_f32_e32 v21, v21, v25
	v_exp_f32_e32 v26, v21
	v_mul_f32_e64 v21, |v23|, s1
	v_fma_f32 v25, v21, s3, 1.0
	v_rcp_f32_e32 v24, v24
	v_rcp_f32_e32 v25, v25
	v_mul_f32_e32 v27, 0xbfb8aa3b, v21
	v_mul_f32_e32 v21, v21, v27
	v_exp_f32_e32 v27, v21
	v_pk_fma_f32 v[28:29], v[24:25], s[0:1], v[36:37] op_sel_hi:[1,0,0]
	v_cmp_le_f32_e32 vcc, 0, v23
	v_pk_fma_f32 v[28:29], v[24:25], v[28:29], s[2:3] op_sel_hi:[1,1,0]
	s_nop 0
	v_pk_fma_f32 v[28:29], v[24:25], v[28:29], s[4:5] op_sel_hi:[1,1,0]
	s_nop 0
	v_pk_fma_f32 v[28:29], v[24:25], v[28:29], s[6:7] op_sel_hi:[1,1,0]
	s_nop 0
	v_pk_mul_f32 v[24:25], v[24:25], v[28:29]
	s_nop 0
	v_pk_mul_f32 v[24:25], v[24:25], 0.5 op_sel_hi:[1,0]
	s_nop 0
	v_pk_mul_f32 v[24:25], v[26:27], v[24:25]
	s_nop 0
	v_pk_mul_f32 v[26:27], v[22:23], v[24:25]
	v_pk_fma_f32 v[24:25], v[22:23], v[24:25], v[22:23] neg_lo:[1,0,0] neg_hi:[1,0,0]
	v_mul_f32_e64 v23, |v17|, s1
	v_cndmask_b32_e32 v21, v27, v25, vcc
	v_cmp_le_f32_e32 vcc, 0, v22
	s_nop 1
	v_cndmask_b32_e32 v22, v26, v24, vcc
	v_cvt_pk_f16_f32 v21, v22, v21
	global_store_dwordx2 v[38:39], v[20:21], off offset:320
	v_mul_f32_e64 v21, |v16|, s1
	v_mul_f32_e32 v22, 0xbfb8aa3b, v21
	v_fma_f32 v20, v21, s3, 1.0
	v_mul_f32_e32 v21, v21, v22
	v_exp_f32_e32 v22, v21
	v_fma_f32 v21, v23, s3, 1.0
	v_rcp_f32_e32 v20, v20
	v_rcp_f32_e32 v21, v21
	v_mul_f32_e32 v24, 0xbfb8aa3b, v23
	v_mul_f32_e32 v23, v23, v24
	v_exp_f32_e32 v23, v23
	v_pk_fma_f32 v[24:25], v[20:21], s[0:1], v[36:37] op_sel_hi:[1,0,0]
	v_cmp_le_f32_e32 vcc, 0, v17
	v_pk_fma_f32 v[24:25], v[20:21], v[24:25], s[2:3] op_sel_hi:[1,1,0]
	s_nop 0
	v_pk_fma_f32 v[24:25], v[20:21], v[24:25], s[4:5] op_sel_hi:[1,1,0]
	s_nop 0
	v_pk_fma_f32 v[24:25], v[20:21], v[24:25], s[6:7] op_sel_hi:[1,1,0]
	s_nop 0
	v_pk_mul_f32 v[20:21], v[20:21], v[24:25]
	s_nop 0
	v_pk_mul_f32 v[20:21], v[20:21], 0.5 op_sel_hi:[1,0]
	s_nop 0
	v_pk_mul_f32 v[20:21], v[22:23], v[20:21]
	s_nop 0
	v_pk_mul_f32 v[22:23], v[16:17], v[20:21]
	v_pk_fma_f32 v[20:21], v[16:17], v[20:21], v[16:17] neg_lo:[1,0,0] neg_hi:[1,0,0]
	s_nop 0
	v_cndmask_b32_e32 v17, v23, v21, vcc
	v_cmp_le_f32_e32 vcc, 0, v16
	s_nop 1
	v_cndmask_b32_e32 v16, v22, v20, vcc
	v_cvt_pk_f16_f32 v16, v16, v17
	v_mul_f32_e64 v17, |v18|, s1
	v_mul_f32_e32 v21, 0xbfb8aa3b, v17
	v_fma_f32 v20, v17, s3, 1.0
	v_mul_f32_e32 v17, v17, v21
	v_exp_f32_e32 v22, v17
	v_mul_f32_e64 v17, |v19|, s1
	v_fma_f32 v21, v17, s3, 1.0
	v_rcp_f32_e32 v20, v20
	v_rcp_f32_e32 v21, v21
	v_mul_f32_e32 v23, 0xbfb8aa3b, v17
	v_mul_f32_e32 v17, v17, v23
	v_exp_f32_e32 v23, v17
	v_pk_fma_f32 v[24:25], v[20:21], s[0:1], v[36:37] op_sel_hi:[1,0,0]
	v_cmp_le_f32_e32 vcc, 0, v19
	v_pk_fma_f32 v[24:25], v[20:21], v[24:25], s[2:3] op_sel_hi:[1,1,0]
	s_nop 0
	v_pk_fma_f32 v[24:25], v[20:21], v[24:25], s[4:5] op_sel_hi:[1,1,0]
	s_nop 0
	v_pk_fma_f32 v[24:25], v[20:21], v[24:25], s[6:7] op_sel_hi:[1,1,0]
	s_nop 0
	v_pk_mul_f32 v[20:21], v[20:21], v[24:25]
	s_nop 0
	v_pk_mul_f32 v[20:21], v[20:21], 0.5 op_sel_hi:[1,0]
	s_nop 0
	v_pk_mul_f32 v[20:21], v[22:23], v[20:21]
	s_nop 0
	v_pk_mul_f32 v[22:23], v[18:19], v[20:21]
	v_pk_fma_f32 v[20:21], v[18:19], v[20:21], v[18:19] neg_lo:[1,0,0] neg_hi:[1,0,0]
	v_mul_f32_e64 v19, |v13|, s1
	v_cndmask_b32_e32 v17, v23, v21, vcc
	v_cmp_le_f32_e32 vcc, 0, v18
	s_nop 1
	v_cndmask_b32_e32 v18, v22, v20, vcc
	v_cvt_pk_f16_f32 v17, v18, v17
	global_store_dwordx2 v[38:39], v[16:17], off offset:448
	v_mul_f32_e64 v17, |v12|, s1
	v_mul_f32_e32 v18, 0xbfb8aa3b, v17
	v_fma_f32 v16, v17, s3, 1.0
	v_mul_f32_e32 v17, v17, v18
	v_exp_f32_e32 v18, v17
	v_fma_f32 v17, v19, s3, 1.0
	v_rcp_f32_e32 v16, v16
	v_rcp_f32_e32 v17, v17
	v_mul_f32_e32 v20, 0xbfb8aa3b, v19
	v_mul_f32_e32 v19, v19, v20
	v_exp_f32_e32 v19, v19
	v_pk_fma_f32 v[20:21], v[16:17], s[0:1], v[36:37] op_sel_hi:[1,0,0]
	v_cmp_le_f32_e32 vcc, 0, v13
	v_pk_fma_f32 v[20:21], v[16:17], v[20:21], s[2:3] op_sel_hi:[1,1,0]
	s_nop 0
	v_pk_fma_f32 v[20:21], v[16:17], v[20:21], s[4:5] op_sel_hi:[1,1,0]
	s_nop 0
	v_pk_fma_f32 v[20:21], v[16:17], v[20:21], s[6:7] op_sel_hi:[1,1,0]
	s_nop 0
	v_pk_mul_f32 v[16:17], v[16:17], v[20:21]
	s_nop 0
	v_pk_mul_f32 v[16:17], v[16:17], 0.5 op_sel_hi:[1,0]
	s_nop 0
	v_pk_mul_f32 v[16:17], v[18:19], v[16:17]
	s_nop 0
	v_pk_mul_f32 v[18:19], v[12:13], v[16:17]
	v_pk_fma_f32 v[16:17], v[12:13], v[16:17], v[12:13] neg_lo:[1,0,0] neg_hi:[1,0,0]
	s_nop 0
	v_cndmask_b32_e32 v13, v19, v17, vcc
	v_cmp_le_f32_e32 vcc, 0, v12
	s_nop 1
	v_cndmask_b32_e32 v12, v18, v16, vcc
	v_cvt_pk_f16_f32 v12, v12, v13
	v_mul_f32_e64 v13, |v14|, s1
	v_mul_f32_e32 v17, 0xbfb8aa3b, v13
	v_fma_f32 v16, v13, s3, 1.0
	v_mul_f32_e32 v13, v13, v17
	v_exp_f32_e32 v18, v13
	v_mul_f32_e64 v13, |v15|, s1
	v_fma_f32 v17, v13, s3, 1.0
	v_rcp_f32_e32 v16, v16
	v_rcp_f32_e32 v17, v17
	v_mul_f32_e32 v19, 0xbfb8aa3b, v13
	v_mul_f32_e32 v13, v13, v19
	v_exp_f32_e32 v19, v13
	v_pk_fma_f32 v[20:21], v[16:17], s[0:1], v[36:37] op_sel_hi:[1,0,0]
	v_cmp_le_f32_e32 vcc, 0, v15
	v_pk_fma_f32 v[20:21], v[16:17], v[20:21], s[2:3] op_sel_hi:[1,1,0]
	s_nop 0
	v_pk_fma_f32 v[20:21], v[16:17], v[20:21], s[4:5] op_sel_hi:[1,1,0]
	s_nop 0
	v_pk_fma_f32 v[20:21], v[16:17], v[20:21], s[6:7] op_sel_hi:[1,1,0]
	s_nop 0
	v_pk_mul_f32 v[16:17], v[16:17], v[20:21]
	s_nop 0
	v_pk_mul_f32 v[16:17], v[16:17], 0.5 op_sel_hi:[1,0]
	s_nop 0
	v_pk_mul_f32 v[16:17], v[18:19], v[16:17]
	s_nop 0
	v_pk_mul_f32 v[18:19], v[14:15], v[16:17]
	v_pk_fma_f32 v[16:17], v[14:15], v[16:17], v[14:15] neg_lo:[1,0,0] neg_hi:[1,0,0]
	v_mul_f32_e64 v15, |v9|, s1
	v_cndmask_b32_e32 v13, v19, v17, vcc
	v_cmp_le_f32_e32 vcc, 0, v14
	s_nop 1
	v_cndmask_b32_e32 v14, v18, v16, vcc
	v_cvt_pk_f16_f32 v13, v14, v13
	global_store_dwordx2 v[38:39], v[12:13], off offset:96
	v_mul_f32_e64 v13, |v8|, s1
	v_mul_f32_e32 v14, 0xbfb8aa3b, v13
	v_fma_f32 v12, v13, s3, 1.0
	v_mul_f32_e32 v13, v13, v14
	v_exp_f32_e32 v14, v13
	v_fma_f32 v13, v15, s3, 1.0
	v_rcp_f32_e32 v12, v12
	v_rcp_f32_e32 v13, v13
	v_mul_f32_e32 v16, 0xbfb8aa3b, v15
	v_mul_f32_e32 v15, v15, v16
	v_exp_f32_e32 v15, v15
	v_pk_fma_f32 v[16:17], v[12:13], s[0:1], v[36:37] op_sel_hi:[1,0,0]
	v_cmp_le_f32_e32 vcc, 0, v9
	v_pk_fma_f32 v[16:17], v[12:13], v[16:17], s[2:3] op_sel_hi:[1,1,0]
	s_nop 0
	v_pk_fma_f32 v[16:17], v[12:13], v[16:17], s[4:5] op_sel_hi:[1,1,0]
	s_nop 0
	v_pk_fma_f32 v[16:17], v[12:13], v[16:17], s[6:7] op_sel_hi:[1,1,0]
	s_nop 0
	v_pk_mul_f32 v[12:13], v[12:13], v[16:17]
	s_nop 0
	v_pk_mul_f32 v[12:13], v[12:13], 0.5 op_sel_hi:[1,0]
	s_nop 0
	v_pk_mul_f32 v[12:13], v[14:15], v[12:13]
	s_nop 0
	v_pk_mul_f32 v[14:15], v[8:9], v[12:13]
	v_pk_fma_f32 v[12:13], v[8:9], v[12:13], v[8:9] neg_lo:[1,0,0] neg_hi:[1,0,0]
	s_nop 0
	v_cndmask_b32_e32 v9, v15, v13, vcc
	v_cmp_le_f32_e32 vcc, 0, v8
	s_nop 1
	v_cndmask_b32_e32 v8, v14, v12, vcc
	v_cvt_pk_f16_f32 v8, v8, v9
	v_mul_f32_e64 v9, |v10|, s1
	v_mul_f32_e32 v13, 0xbfb8aa3b, v9
	v_fma_f32 v12, v9, s3, 1.0
	v_mul_f32_e32 v9, v9, v13
	v_exp_f32_e32 v14, v9
	v_mul_f32_e64 v9, |v11|, s1
	v_fma_f32 v13, v9, s3, 1.0
	v_rcp_f32_e32 v12, v12
	v_rcp_f32_e32 v13, v13
	v_mul_f32_e32 v15, 0xbfb8aa3b, v9
	v_mul_f32_e32 v9, v9, v15
	v_exp_f32_e32 v15, v9
	v_pk_fma_f32 v[16:17], v[12:13], s[0:1], v[36:37] op_sel_hi:[1,0,0]
	v_cmp_le_f32_e32 vcc, 0, v11
	v_pk_fma_f32 v[16:17], v[12:13], v[16:17], s[2:3] op_sel_hi:[1,1,0]
	s_nop 0
	v_pk_fma_f32 v[16:17], v[12:13], v[16:17], s[4:5] op_sel_hi:[1,1,0]
	s_nop 0
	v_pk_fma_f32 v[16:17], v[12:13], v[16:17], s[6:7] op_sel_hi:[1,1,0]
	s_nop 0
	v_pk_mul_f32 v[12:13], v[12:13], v[16:17]
	s_nop 0
	v_pk_mul_f32 v[12:13], v[12:13], 0.5 op_sel_hi:[1,0]
	s_nop 0
	v_pk_mul_f32 v[12:13], v[14:15], v[12:13]
	s_nop 0
	v_pk_mul_f32 v[14:15], v[10:11], v[12:13]
	v_pk_fma_f32 v[12:13], v[10:11], v[12:13], v[10:11] neg_lo:[1,0,0] neg_hi:[1,0,0]
	v_mul_f32_e64 v11, |v5|, s1
	v_cndmask_b32_e32 v9, v15, v13, vcc
	v_cmp_le_f32_e32 vcc, 0, v10
	s_nop 1
	v_cndmask_b32_e32 v10, v14, v12, vcc
	v_cvt_pk_f16_f32 v9, v10, v9
	global_store_dwordx2 v[38:39], v[8:9], off offset:224
	v_mul_f32_e64 v9, |v4|, s1
	v_mul_f32_e32 v10, 0xbfb8aa3b, v9
	v_fma_f32 v8, v9, s3, 1.0
	v_mul_f32_e32 v9, v9, v10
	v_exp_f32_e32 v10, v9
	v_fma_f32 v9, v11, s3, 1.0
	v_rcp_f32_e32 v8, v8
	v_rcp_f32_e32 v9, v9
	v_mul_f32_e32 v12, 0xbfb8aa3b, v11
	v_mul_f32_e32 v11, v11, v12
	v_exp_f32_e32 v11, v11
	v_pk_fma_f32 v[12:13], v[8:9], s[0:1], v[36:37] op_sel_hi:[1,0,0]
	v_cmp_le_f32_e32 vcc, 0, v5
	v_pk_fma_f32 v[12:13], v[8:9], v[12:13], s[2:3] op_sel_hi:[1,1,0]
	s_nop 0
	v_pk_fma_f32 v[12:13], v[8:9], v[12:13], s[4:5] op_sel_hi:[1,1,0]
	s_nop 0
	v_pk_fma_f32 v[12:13], v[8:9], v[12:13], s[6:7] op_sel_hi:[1,1,0]
	s_nop 0
	v_pk_mul_f32 v[8:9], v[8:9], v[12:13]
	s_nop 0
	v_pk_mul_f32 v[8:9], v[8:9], 0.5 op_sel_hi:[1,0]
	s_nop 0
	v_pk_mul_f32 v[8:9], v[10:11], v[8:9]
	s_nop 0
	v_pk_mul_f32 v[10:11], v[4:5], v[8:9]
	v_pk_fma_f32 v[8:9], v[4:5], v[8:9], v[4:5] neg_lo:[1,0,0] neg_hi:[1,0,0]
	s_nop 0
	v_cndmask_b32_e32 v5, v11, v9, vcc
	v_cmp_le_f32_e32 vcc, 0, v4
	s_nop 1
	v_cndmask_b32_e32 v4, v10, v8, vcc
	v_cvt_pk_f16_f32 v4, v4, v5
	v_mul_f32_e64 v5, |v6|, s1
	v_mul_f32_e32 v9, 0xbfb8aa3b, v5
	v_fma_f32 v8, v5, s3, 1.0
	v_mul_f32_e32 v5, v5, v9
	v_exp_f32_e32 v10, v5
	v_mul_f32_e64 v5, |v7|, s1
	v_fma_f32 v9, v5, s3, 1.0
	v_rcp_f32_e32 v8, v8
	v_rcp_f32_e32 v9, v9
	v_mul_f32_e32 v11, 0xbfb8aa3b, v5
	v_mul_f32_e32 v5, v5, v11
	v_exp_f32_e32 v11, v5
	v_pk_fma_f32 v[12:13], v[8:9], s[0:1], v[36:37] op_sel_hi:[1,0,0]
	v_cmp_le_f32_e32 vcc, 0, v7
	v_pk_fma_f32 v[12:13], v[8:9], v[12:13], s[2:3] op_sel_hi:[1,1,0]
	s_nop 0
	v_pk_fma_f32 v[12:13], v[8:9], v[12:13], s[4:5] op_sel_hi:[1,1,0]
	s_nop 0
	v_pk_fma_f32 v[12:13], v[8:9], v[12:13], s[6:7] op_sel_hi:[1,1,0]
	s_nop 0
	v_pk_mul_f32 v[8:9], v[8:9], v[12:13]
	s_nop 0
	v_pk_mul_f32 v[8:9], v[8:9], 0.5 op_sel_hi:[1,0]
	s_nop 0
	v_pk_mul_f32 v[8:9], v[10:11], v[8:9]
	s_nop 0
	v_pk_mul_f32 v[10:11], v[6:7], v[8:9]
	v_pk_fma_f32 v[8:9], v[6:7], v[8:9], v[6:7] neg_lo:[1,0,0] neg_hi:[1,0,0]
	v_mul_f32_e64 v7, |v1|, s1
	v_cndmask_b32_e32 v5, v11, v9, vcc
	v_cmp_le_f32_e32 vcc, 0, v6
	s_nop 1
	v_cndmask_b32_e32 v6, v10, v8, vcc
	v_cvt_pk_f16_f32 v5, v6, v5
	global_store_dwordx2 v[38:39], v[4:5], off offset:352
	v_mul_f32_e64 v5, |v0|, s1
	v_mul_f32_e32 v6, 0xbfb8aa3b, v5
	v_fma_f32 v4, v5, s3, 1.0
	v_mul_f32_e32 v5, v5, v6
	v_exp_f32_e32 v6, v5
	v_fma_f32 v5, v7, s3, 1.0
	v_rcp_f32_e32 v4, v4
	v_rcp_f32_e32 v5, v5
	v_mul_f32_e32 v8, 0xbfb8aa3b, v7
	v_mul_f32_e32 v7, v7, v8
	v_exp_f32_e32 v7, v7
	v_pk_fma_f32 v[8:9], v[4:5], s[0:1], v[36:37] op_sel_hi:[1,0,0]
	v_cmp_le_f32_e32 vcc, 0, v1
	v_pk_fma_f32 v[8:9], v[4:5], v[8:9], s[2:3] op_sel_hi:[1,1,0]
	s_nop 0
	v_pk_fma_f32 v[8:9], v[4:5], v[8:9], s[4:5] op_sel_hi:[1,1,0]
	s_nop 0
	v_pk_fma_f32 v[8:9], v[4:5], v[8:9], s[6:7] op_sel_hi:[1,1,0]
	s_nop 0
	v_pk_mul_f32 v[4:5], v[4:5], v[8:9]
	s_nop 0
	v_pk_mul_f32 v[4:5], v[4:5], 0.5 op_sel_hi:[1,0]
	s_nop 0
	v_pk_mul_f32 v[4:5], v[6:7], v[4:5]
	s_nop 0
	v_pk_mul_f32 v[6:7], v[0:1], v[4:5]
	v_pk_fma_f32 v[4:5], v[0:1], v[4:5], v[0:1] neg_lo:[1,0,0] neg_hi:[1,0,0]
	s_nop 0
	v_cndmask_b32_e32 v1, v7, v5, vcc
	v_cmp_le_f32_e32 vcc, 0, v0
	s_nop 1
	v_cndmask_b32_e32 v0, v6, v4, vcc
	v_cvt_pk_f16_f32 v0, v0, v1
	v_mul_f32_e64 v1, |v2|, s1
	v_mul_f32_e32 v5, 0xbfb8aa3b, v1
	v_fma_f32 v4, v1, s3, 1.0
	v_mul_f32_e32 v1, v1, v5
	v_exp_f32_e32 v6, v1
	v_mul_f32_e64 v1, |v3|, s1
	v_fma_f32 v5, v1, s3, 1.0
	v_rcp_f32_e32 v4, v4
	v_rcp_f32_e32 v5, v5
	v_mul_f32_e32 v7, 0xbfb8aa3b, v1
	v_mul_f32_e32 v1, v1, v7
	v_exp_f32_e32 v7, v1
	v_pk_fma_f32 v[8:9], v[4:5], s[0:1], v[36:37] op_sel_hi:[1,0,0]
	v_cmp_le_f32_e32 vcc, 0, v3
	v_pk_fma_f32 v[8:9], v[4:5], v[8:9], s[2:3] op_sel_hi:[1,1,0]
	s_nop 0
	v_pk_fma_f32 v[8:9], v[4:5], v[8:9], s[4:5] op_sel_hi:[1,1,0]
	s_nop 0
	v_pk_fma_f32 v[8:9], v[4:5], v[8:9], s[6:7] op_sel_hi:[1,1,0]
	s_nop 0
	v_pk_mul_f32 v[4:5], v[4:5], v[8:9]
	s_nop 0
	v_pk_mul_f32 v[4:5], v[4:5], 0.5 op_sel_hi:[1,0]
	s_nop 0
	v_pk_mul_f32 v[4:5], v[6:7], v[4:5]
	s_nop 0
	v_pk_mul_f32 v[6:7], v[2:3], v[4:5]
	v_pk_fma_f32 v[4:5], v[2:3], v[4:5], v[2:3] neg_lo:[1,0,0] neg_hi:[1,0,0]
	s_nop 0
	v_cndmask_b32_e32 v1, v7, v5, vcc
	v_cmp_le_f32_e32 vcc, 0, v2
	s_nop 1
	v_cndmask_b32_e32 v2, v6, v4, vcc
	v_cvt_pk_f16_f32 v1, v2, v1
	global_store_dwordx2 v[38:39], v[0:1], off offset:480
	s_endpgm
